# speedup vs baseline: 1.0212x; 1.0018x over previous
_Z16bilateral_kernelPKfS0_Pf:
	s_load_dwordx2 s[4:5], s[0:1], 0x0
	s_load_dwordx2 s[8:9], s[0:1], 0x10
	s_lshr_b32 s19, s2, 8
	s_and_b32 s0, s2, 7
	s_mulk_i32 s0, 0x60
	s_lshr_b32 s1, s2, 3
	s_add_i32 s1, s0, s1
	s_lshr_b32 s0, s1, 6
	s_lshl_b32 s11, s1, 6
	s_nop 0
	s_and_b32 s11, s11, 0x1c0
	s_lshl_b32 s1, s1, 3
	s_nop 0
	s_and_b32 s10, s1, 0x1c0
	s_mov_b32 s1, 0
	s_lshl_b64 s[2:3], s[0:1], 20
	s_mov_b32 s20, 0xc05dfbe6
	s_mov_b32 s21, 0xc05dfbe6
	s_mov_b32 s22, 0xc0a8390e
	s_mov_b32 s23, 0xc0a8390e
	s_mov_b32 s24, 0xc08211a7
	s_mov_b32 s25, 0xc08211a7
	s_mov_b32 s26, 0xc0bb4cc1
	s_mov_b32 s27, 0xc0bb4cc1
	s_mov_b32 s28, 0xc0f487dc
	s_mov_b32 s29, 0xc0f487dc
	s_mov_b32 s30, 0x3e0bd796
	s_mov_b32 s31, 0x3e0bd796
	s_mov_b32 s32, 0x3f45a90c
	s_mov_b32 s33, 0x3f45a90c
	s_mov_b32 s34, 0x3fa5c782
	s_mov_b32 s35, 0x3fa5c782
	v_and_b32_e32 v118, 15, v0
	v_lshrrev_b32_e32 v115, 2, v0
	v_lshl_or_b32 v113, v118, 2, s11
	v_and_or_b32 v117, v115, 60, s10
	v_min_u32_e32 v116, 0x1fa, v113
	v_sub_u32_e64 v115, v113, 2 clamp
	v_add_u32_e64 v116, 4, v116
	v_cmp_eq_u32_e64 s[16:17], 0, v118
	v_cmp_eq_u32_e32 vcc, 15, v118
	s_nop 1
	v_cndmask_b32_e64 v115, v116, v115, s[16:17]
	s_or_b64 vcc, s[16:17], vcc
	v_lshlrev_b32_e32 v115, 2, v115
	v_mov_b32_e32 v116, 0x7ff00000
	s_nop 0
	v_cndmask_b32_e32 v112, v116, v115, vcc
	s_movk_i32 s18, 0x1fc
	v_cmp_eq_u32_e32 vcc, 0, v113
	v_cmp_eq_u32_e64 s[16:17], s18, v113
	v_lshlrev_b32_e32 v113, 2, v113
	s_waitcnt lgkmcnt(0)
	s_add_u32 s4, s4, s2
	s_addc_u32 s5, s5, s3
	s_and_b32 s5, s5, 0xffff
	s_mov_b32 s6, 0x100000
	s_mov_b32 s7, 0x20000
	s_add_u32 s12, s8, s2
	s_addc_u32 s13, s9, s3
	s_and_b32 s13, s13, 0xffff
	s_mov_b32 s14, 0x100000
	s_mov_b32 s15, 0x20000
	v_sub_u32_e64 v115, v117, 2 clamp
	v_lshlrev_b32_e32 v115, 11, v115
	v_add_u32_e32 v116, v115, v112
	v_add_u32_e64 v115, v115, v113
	buffer_load_dwordx2 v[0:1], v116, s[4:7], 0 offen nt
	buffer_load_dwordx2 v[6:7], v116, s[4:7], 0 offen nt
	buffer_load_dwordx4 v[2:5], v115, s[4:7], 0 offen nt
	v_sub_u32_e64 v115, v117, 1 clamp
	v_lshlrev_b32_e32 v115, 11, v115
	v_add_u32_e32 v116, v115, v112
	v_add_u32_e64 v115, v115, v113
	buffer_load_dwordx2 v[8:9], v116, s[4:7], 0 offen nt
	buffer_load_dwordx2 v[14:15], v116, s[4:7], 0 offen nt
	buffer_load_dwordx4 v[10:13], v115, s[4:7], 0 offen nt
	v_lshlrev_b32_e32 v115, 11, v117
	v_add_u32_e32 v116, v115, v112
	v_add_u32_e64 v114, v115, v113
	v_add_u32_e32 v119, 0x1000, v114
	buffer_load_dwordx2 v[16:17], v116, s[4:7], 0 offen nt
	buffer_load_dwordx2 v[22:23], v116, s[4:7], 0 offen nt
	buffer_load_dwordx4 v[18:21], v114, s[4:7], 0 offen nt
	v_lshlrev_b32_e64 v115, 11, v117
	v_add_u32_e32 v115, 0x800, v115
	v_add_u32_e32 v116, v115, v112
	v_add_u32_e32 v115, v115, v113
	buffer_load_dwordx2 v[24:25], v116, s[4:7], 0 offen nt
	buffer_load_dwordx2 v[30:31], v116, s[4:7], 0 offen nt
	buffer_load_dwordx4 v[26:29], v115, s[4:7], 0 offen nt
	v_lshlrev_b32_e64 v115, 11, v117
	v_add_u32_e32 v115, 0x1000, v115
	v_add_u32_e32 v116, v115, v112
	v_add_u32_e32 v115, v115, v113
	buffer_load_dwordx2 v[32:33], v116, s[4:7], 0 offen nt
	buffer_load_dwordx2 v[38:39], v116, s[4:7], 0 offen nt
	buffer_load_dwordx4 v[34:37], v115, s[4:7], 0 offen nt
	v_lshlrev_b32_e64 v115, 11, v117
	v_add_u32_e32 v115, 0x1800, v115
	v_add_u32_e32 v116, v115, v112
	v_add_u32_e32 v115, v115, v113
	buffer_load_dwordx2 v[40:41], v116, s[4:7], 0 offen nt
	buffer_load_dwordx2 v[46:47], v116, s[4:7], 0 offen nt
	buffer_load_dwordx4 v[42:45], v115, s[4:7], 0 offen nt
	v_min_u32_e32 v115, 0x1fb, v117
	v_lshlrev_b32_e64 v115, 11, v115
	v_add_u32_e32 v115, 0x2000, v115
	v_add_u32_e32 v116, v115, v112
	v_add_u32_e32 v115, v115, v113
	buffer_load_dwordx2 v[48:49], v116, s[4:7], 0 offen nt
	buffer_load_dwordx2 v[54:55], v116, s[4:7], 0 offen nt
	buffer_load_dwordx4 v[50:53], v115, s[4:7], 0 offen nt
	v_min_u32_e32 v115, 0x1fa, v117
	v_lshlrev_b32_e64 v115, 11, v115
	v_add_u32_e32 v115, 0x2800, v115
	v_add_u32_e32 v116, v115, v112
	v_add_u32_e32 v115, v115, v113
	buffer_load_dwordx2 v[56:57], v116, s[4:7], 0 offen nt
	buffer_load_dwordx2 v[62:63], v116, s[4:7], 0 offen nt
	buffer_load_dwordx4 v[58:61], v115, s[4:7], 0 offen nt
	s_cmp_eq_u32 s19, 0
	s_cbranch_scc1 .Lmyp0
	s_cmp_eq_u32 s19, 1
	s_cbranch_scc1 .Lmyp1
	s_setprio 0
	s_branch .Lmypd
.Lmyp1:
	s_setprio 1
	s_branch .Lmypd
.Lmyp0:
	s_setprio 2
.Lmypd:
	s_waitcnt vmcnt(21)
	v_mov_b32_dpp v0, v4 row_shr:1 row_mask:0xf bank_mask:0xf
	v_mov_b32_dpp v1, v5 row_shr:1 row_mask:0xf bank_mask:0xf
	v_mov_b32_dpp v6, v2 row_shl:1 row_mask:0xf bank_mask:0xf
	v_mov_b32_dpp v7, v3 row_shl:1 row_mask:0xf bank_mask:0xf
	v_pk_mul_f32 v[2:3], v[2:3], s[32:33]
	v_pk_mul_f32 v[4:5], v[4:5], s[32:33]
	v_cndmask_b32_e64 v1, v1, v0, vcc
	v_cndmask_b32_e64 v6, v6, v7, s[16:17]
	v_pk_mul_f32 v[0:1], v[0:1], s[32:33]
	v_pk_mul_f32 v[6:7], v[6:7], s[32:33]
	s_waitcnt vmcnt(18)
	s_nop 0
	v_mov_b32_dpp v8, v12 row_shr:1 row_mask:0xf bank_mask:0xf
	v_mov_b32_dpp v9, v13 row_shr:1 row_mask:0xf bank_mask:0xf
	v_mov_b32_dpp v14, v10 row_shl:1 row_mask:0xf bank_mask:0xf
	v_mov_b32_dpp v15, v11 row_shl:1 row_mask:0xf bank_mask:0xf
	v_pk_mul_f32 v[10:11], v[10:11], s[32:33]
	v_pk_mul_f32 v[12:13], v[12:13], s[32:33]
	v_cndmask_b32_e64 v9, v9, v8, vcc
	v_cndmask_b32_e64 v14, v14, v15, s[16:17]
	v_pk_mul_f32 v[8:9], v[8:9], s[32:33]
	v_pk_mul_f32 v[14:15], v[14:15], s[32:33]
	s_waitcnt vmcnt(15)
	s_nop 0
	v_mov_b32_dpp v16, v20 row_shr:1 row_mask:0xf bank_mask:0xf
	v_mov_b32_dpp v17, v21 row_shr:1 row_mask:0xf bank_mask:0xf
	v_mov_b32_dpp v22, v18 row_shl:1 row_mask:0xf bank_mask:0xf
	v_mov_b32_dpp v23, v19 row_shl:1 row_mask:0xf bank_mask:0xf
	v_pk_mul_f32 v[18:19], v[18:19], s[32:33]
	v_pk_mul_f32 v[20:21], v[20:21], s[32:33]
	v_cndmask_b32_e64 v17, v17, v16, vcc
	v_cndmask_b32_e64 v22, v22, v23, s[16:17]
	v_pk_mul_f32 v[68:69], v[18:19], s[30:31]
	v_pk_mul_f32 v[70:71], v[20:21], s[30:31]
	v_pk_mul_f32 v[16:17], v[16:17], s[32:33]
	v_pk_mul_f32 v[22:23], v[22:23], s[32:33]
	v_pk_add_f32 v[96:97], v[18:19], v[0:1] neg_lo:[0,1] neg_hi:[0,1]
	v_pk_add_f32 v[98:99], v[18:19], v[2:3] neg_lo:[0,1] neg_hi:[0,1]
	v_pk_add_f32 v[100:101], v[20:21], v[2:3] neg_lo:[0,1] neg_hi:[0,1]
	v_pk_add_f32 v[102:103], v[18:19], v[4:5] neg_lo:[0,1] neg_hi:[0,1]
	v_pk_fma_f32 v[96:97], v[96:97], v[96:97], s[28:29] neg_lo:[1,0,0] neg_hi:[1,0,0]
	v_pk_fma_f32 v[98:99], v[98:99], v[98:99], s[22:23] neg_lo:[1,0,0] neg_hi:[1,0,0]
	v_pk_fma_f32 v[100:101], v[100:101], v[100:101], s[28:29] neg_lo:[1,0,0] neg_hi:[1,0,0]
	v_pk_fma_f32 v[102:103], v[102:103], v[102:103], s[28:29] neg_lo:[1,0,0] neg_hi:[1,0,0]
	v_exp_f32_e32 v96, v96
	v_exp_f32_e32 v97, v97
	v_exp_f32_e32 v98, v98
	v_exp_f32_e32 v99, v99
	v_exp_f32_e32 v100, v100
	v_exp_f32_e32 v101, v101
	v_exp_f32_e32 v102, v102
	v_exp_f32_e32 v103, v103
	v_pk_add_f32 v[104:105], v[20:21], v[4:5] neg_lo:[0,1] neg_hi:[0,1]
	v_pk_add_f32 v[106:107], v[20:21], v[6:7] neg_lo:[0,1] neg_hi:[0,1]
	v_pk_add_f32 v[108:109], v[18:19], v[2:3] op_sel:[1,0] op_sel_hi:[0,1] neg_lo:[0,1] neg_hi:[0,1]
	v_pk_add_f32 v[110:111], v[20:21], v[4:5] op_sel:[1,0] op_sel_hi:[0,1] neg_lo:[0,1] neg_hi:[0,1]
	v_pk_fma_f32 v[104:105], v[104:105], v[104:105], s[22:23] neg_lo:[1,0,0] neg_hi:[1,0,0]
	v_pk_fma_f32 v[106:107], v[106:107], v[106:107], s[28:29] neg_lo:[1,0,0] neg_hi:[1,0,0]
	v_pk_fma_f32 v[108:109], v[108:109], v[108:109], s[26:27] neg_lo:[1,0,0] neg_hi:[1,0,0]
	v_pk_fma_f32 v[110:111], v[110:111], v[110:111], s[26:27] neg_lo:[1,0,0] neg_hi:[1,0,0]
	v_exp_f32_e32 v104, v104
	v_exp_f32_e32 v105, v105
	v_exp_f32_e32 v106, v106
	v_exp_f32_e32 v107, v107
	v_exp_f32_e32 v108, v108
	v_exp_f32_e32 v109, v109
	v_exp_f32_e32 v110, v110
	v_exp_f32_e32 v111, v111
	v_pk_add_f32 v[64:65], s[30:31], v[96:97]
	v_pk_fma_f32 v[68:69], v[96:97], v[0:1], v[68:69]
	v_pk_add_f32 v[66:67], s[30:31], v[100:101]
	v_pk_add_f32 v[64:65], v[64:65], v[98:99]
	v_pk_fma_f32 v[68:69], v[98:99], v[2:3], v[68:69]
	v_pk_fma_f32 v[70:71], v[100:101], v[2:3], v[70:71]
	v_pk_add_f32 v[64:65], v[64:65], v[102:103]
	v_pk_fma_f32 v[68:69], v[102:103], v[4:5], v[68:69]
	v_pk_add_f32 v[96:97], v[18:19], v[8:9] neg_lo:[0,1] neg_hi:[0,1]
	v_pk_add_f32 v[98:99], v[18:19], v[10:11] neg_lo:[0,1] neg_hi:[0,1]
	v_pk_add_f32 v[100:101], v[20:21], v[10:11] neg_lo:[0,1] neg_hi:[0,1]
	v_pk_add_f32 v[102:103], v[18:19], v[12:13] neg_lo:[0,1] neg_hi:[0,1]
	v_pk_fma_f32 v[96:97], v[96:97], v[96:97], s[26:27] neg_lo:[1,0,0] neg_hi:[1,0,0]
	v_pk_fma_f32 v[98:99], v[98:99], v[98:99], s[20:21] neg_lo:[1,0,0] neg_hi:[1,0,0]
	v_pk_fma_f32 v[100:101], v[100:101], v[100:101], s[26:27] neg_lo:[1,0,0] neg_hi:[1,0,0]
	v_pk_fma_f32 v[102:103], v[102:103], v[102:103], s[26:27] neg_lo:[1,0,0] neg_hi:[1,0,0]
	v_exp_f32_e32 v96, v96
	v_exp_f32_e32 v97, v97
	v_exp_f32_e32 v98, v98
	v_exp_f32_e32 v99, v99
	v_exp_f32_e32 v100, v100
	v_exp_f32_e32 v101, v101
	v_exp_f32_e32 v102, v102
	v_exp_f32_e32 v103, v103
	v_pk_add_f32 v[66:67], v[66:67], v[104:105]
	v_pk_fma_f32 v[70:71], v[104:105], v[4:5], v[70:71]
	v_pk_add_f32 v[64:65], v[64:65], v[108:109] op_sel:[0,1] op_sel_hi:[1,0]
	v_pk_add_f32 v[66:67], v[66:67], v[106:107]
	v_pk_fma_f32 v[70:71], v[106:107], v[6:7], v[70:71]
	v_pk_fma_f32 v[68:69], v[108:109], v[2:3], v[68:69] op_sel:[1,1,0] op_sel_hi:[0,0,1]
	v_pk_add_f32 v[66:67], v[66:67], v[110:111] op_sel:[0,1] op_sel_hi:[1,0]
	v_pk_fma_f32 v[70:71], v[110:111], v[4:5], v[70:71] op_sel:[1,1,0] op_sel_hi:[0,0,1]
	v_pk_add_f32 v[104:105], v[20:21], v[12:13] neg_lo:[0,1] neg_hi:[0,1]
	v_pk_add_f32 v[106:107], v[20:21], v[14:15] neg_lo:[0,1] neg_hi:[0,1]
	v_pk_add_f32 v[108:109], v[18:19], v[10:11] op_sel:[1,0] op_sel_hi:[0,1] neg_lo:[0,1] neg_hi:[0,1]
	v_pk_add_f32 v[110:111], v[20:21], v[12:13] op_sel:[1,0] op_sel_hi:[0,1] neg_lo:[0,1] neg_hi:[0,1]
	v_pk_fma_f32 v[104:105], v[104:105], v[104:105], s[20:21] neg_lo:[1,0,0] neg_hi:[1,0,0]
	v_pk_fma_f32 v[106:107], v[106:107], v[106:107], s[26:27] neg_lo:[1,0,0] neg_hi:[1,0,0]
	v_pk_fma_f32 v[108:109], v[108:109], v[108:109], s[24:25] neg_lo:[1,0,0] neg_hi:[1,0,0]
	v_pk_fma_f32 v[110:111], v[110:111], v[110:111], s[24:25] neg_lo:[1,0,0] neg_hi:[1,0,0]
	v_exp_f32_e32 v104, v104
	v_exp_f32_e32 v105, v105
	v_exp_f32_e32 v106, v106
	v_exp_f32_e32 v107, v107
	v_exp_f32_e32 v108, v108
	v_exp_f32_e32 v109, v109
	v_exp_f32_e32 v110, v110
	v_exp_f32_e32 v111, v111
	v_pk_add_f32 v[64:65], v[64:65], v[96:97]
	v_pk_fma_f32 v[68:69], v[96:97], v[8:9], v[68:69]
	v_pk_add_f32 v[66:67], v[66:67], v[100:101]
	v_pk_add_f32 v[64:65], v[64:65], v[98:99]
	v_pk_fma_f32 v[68:69], v[98:99], v[10:11], v[68:69]
	v_pk_fma_f32 v[70:71], v[100:101], v[10:11], v[70:71]
	v_pk_add_f32 v[64:65], v[64:65], v[102:103]
	v_pk_fma_f32 v[68:69], v[102:103], v[12:13], v[68:69]
	v_pk_add_f32 v[96:97], v[18:19], v[16:17] neg_lo:[0,1] neg_hi:[0,1]
	v_pk_add_f32 v[98:99], v[20:21], v[18:19] neg_lo:[0,1] neg_hi:[0,1]
	v_pk_add_f32 v[100:101], v[22:23], v[20:21] neg_lo:[0,1] neg_hi:[0,1]
	v_pk_fma_f32 v[96:97], v[96:97], v[96:97], s[22:23] neg_lo:[1,0,0] neg_hi:[1,0,0]
	v_pk_fma_f32 v[98:99], v[98:99], v[98:99], s[22:23] neg_lo:[1,0,0] neg_hi:[1,0,0]
	v_pk_fma_f32 v[100:101], v[100:101], v[100:101], s[22:23] neg_lo:[1,0,0] neg_hi:[1,0,0]
	v_exp_f32_e32 v96, v96
	v_exp_f32_e32 v97, v97
	v_exp_f32_e32 v98, v98
	v_exp_f32_e32 v99, v99
	v_exp_f32_e32 v100, v100
	v_exp_f32_e32 v101, v101
	v_pk_add_f32 v[66:67], v[66:67], v[104:105]
	v_pk_fma_f32 v[70:71], v[104:105], v[12:13], v[70:71]
	v_pk_add_f32 v[64:65], v[64:65], v[108:109] op_sel:[0,1] op_sel_hi:[1,0]
	v_pk_add_f32 v[66:67], v[66:67], v[106:107]
	v_pk_fma_f32 v[70:71], v[106:107], v[14:15], v[70:71]
	v_pk_fma_f32 v[68:69], v[108:109], v[10:11], v[68:69] op_sel:[1,1,0] op_sel_hi:[0,0,1]
	v_pk_add_f32 v[66:67], v[66:67], v[110:111] op_sel:[0,1] op_sel_hi:[1,0]
	v_pk_fma_f32 v[70:71], v[110:111], v[12:13], v[70:71] op_sel:[1,1,0] op_sel_hi:[0,0,1]
	v_sub_f32_e32 v104, v18, v1
	v_sub_f32_e32 v106, v20, v3
	v_sub_f32_e32 v108, v19, v4
	v_sub_f32_e32 v110, v21, v6
	v_sub_f32_e32 v105, v18, v9
	v_sub_f32_e32 v107, v20, v11
	v_sub_f32_e32 v109, v19, v12
	v_sub_f32_e32 v111, v21, v14
	v_fma_f32 v104, -v104, v104, s26
	v_fma_f32 v106, -v106, v106, s26
	v_fma_f32 v108, -v108, v108, s26
	v_fma_f32 v110, -v110, v110, s26
	v_fma_f32 v105, -v105, v105, s24
	v_fma_f32 v107, -v107, v107, s24
	v_fma_f32 v109, -v109, v109, s24
	v_fma_f32 v111, -v111, v111, s24
	v_exp_f32_e32 v104, v104
	v_exp_f32_e32 v106, v106
	v_exp_f32_e32 v108, v108
	v_exp_f32_e32 v110, v110
	v_exp_f32_e32 v105, v105
	v_exp_f32_e32 v107, v107
	v_exp_f32_e32 v109, v109
	v_exp_f32_e32 v111, v111
	v_pk_add_f32 v[64:65], v[64:65], v[96:97]
	v_pk_fma_f32 v[68:69], v[96:97], v[16:17], v[68:69]
	v_pk_add_f32 v[66:67], v[66:67], v[98:99]
	v_pk_add_f32 v[64:65], v[64:65], v[98:99]
	v_pk_fma_f32 v[68:69], v[98:99], v[20:21], v[68:69]
	v_pk_fma_f32 v[70:71], v[98:99], v[18:19], v[70:71]
	v_pk_add_f32 v[66:67], v[66:67], v[100:101]
	v_pk_fma_f32 v[70:71], v[100:101], v[22:23], v[70:71]
	v_sub_f32_e32 v100, v18, v17
	v_sub_f32_e32 v96, v19, v18
	v_sub_f32_e32 v102, v20, v19
	v_sub_f32_e32 v98, v21, v20
	v_sub_f32_e64 v97, v22, v21
	v_fma_f32 v100, -v100, v100, s20
	v_fma_f32 v96, -v96, v96, s20
	v_fma_f32 v102, -v102, v102, s20
	v_fma_f32 v98, -v98, v98, s20
	v_fma_f32 v97, -v97, v97, s20
	v_exp_f32_e32 v100, v100
	v_exp_f32_e32 v96, v96
	v_exp_f32_e32 v102, v102
	v_exp_f32_e32 v98, v98
	v_exp_f32_e32 v97, v97
	v_add_f32_e32 v64, v64, v104
	v_fmac_f32_e32 v68, v104, v1
	v_add_f32_e32 v66, v66, v106
	v_fmac_f32_e32 v70, v106, v3
	v_add_f32_e32 v65, v65, v108
	v_fmac_f32_e32 v69, v108, v4
	v_add_f32_e32 v67, v67, v110
	v_fmac_f32_e32 v71, v110, v6
	v_add_f32_e32 v64, v64, v105
	v_fmac_f32_e32 v68, v105, v9
	v_add_f32_e32 v66, v66, v107
	v_fmac_f32_e32 v70, v107, v11
	v_add_f32_e32 v65, v65, v109
	v_fmac_f32_e32 v69, v109, v12
	v_add_f32_e32 v67, v67, v111
	v_fmac_f32_e32 v71, v111, v14
	v_add_f32_e32 v64, v64, v100
	v_fmac_f32_e32 v68, v100, v17
	v_add_f32_e32 v65, v65, v102
	v_fmac_f32_e32 v69, v102, v20
	v_add_f32_e32 v66, v66, v102
	v_fmac_f32_e32 v70, v102, v19
	v_add_f32_e32 v67, v67, v97
	v_fmac_f32_e64 v71, v97, v22
	v_pk_add_f32 v[64:65], v[64:65], v[96:97] op_sel_hi:[1,0]
	v_pk_fma_f32 v[68:69], v[96:97], v[18:19], v[68:69] op_sel:[0,1,0] op_sel_hi:[0,0,1]
	v_pk_add_f32 v[66:67], v[66:67], v[98:99] op_sel_hi:[1,0]
	v_pk_fma_f32 v[70:71], v[98:99], v[20:21], v[70:71] op_sel:[0,1,0] op_sel_hi:[0,0,1]
	s_waitcnt vmcnt(12)
	s_nop 0
	v_mov_b32_dpp v24, v28 row_shr:1 row_mask:0xf bank_mask:0xf
	v_mov_b32_dpp v25, v29 row_shr:1 row_mask:0xf bank_mask:0xf
	v_mov_b32_dpp v30, v26 row_shl:1 row_mask:0xf bank_mask:0xf
	v_mov_b32_dpp v31, v27 row_shl:1 row_mask:0xf bank_mask:0xf
	v_pk_mul_f32 v[26:27], v[26:27], s[32:33]
	v_pk_mul_f32 v[28:29], v[28:29], s[32:33]
	v_cndmask_b32_e64 v25, v25, v24, vcc
	v_cndmask_b32_e64 v30, v30, v31, s[16:17]
	v_pk_mul_f32 v[76:77], v[26:27], s[30:31]
	v_pk_mul_f32 v[78:79], v[28:29], s[30:31]
	v_pk_mul_f32 v[24:25], v[24:25], s[32:33]
	v_pk_mul_f32 v[30:31], v[30:31], s[32:33]
	v_pk_add_f32 v[96:97], v[26:27], v[8:9] neg_lo:[0,1] neg_hi:[0,1]
	v_pk_add_f32 v[98:99], v[26:27], v[10:11] neg_lo:[0,1] neg_hi:[0,1]
	v_pk_add_f32 v[100:101], v[28:29], v[10:11] neg_lo:[0,1] neg_hi:[0,1]
	v_pk_add_f32 v[102:103], v[26:27], v[12:13] neg_lo:[0,1] neg_hi:[0,1]
	v_pk_fma_f32 v[96:97], v[96:97], v[96:97], s[28:29] neg_lo:[1,0,0] neg_hi:[1,0,0]
	v_pk_fma_f32 v[98:99], v[98:99], v[98:99], s[22:23] neg_lo:[1,0,0] neg_hi:[1,0,0]
	v_pk_fma_f32 v[100:101], v[100:101], v[100:101], s[28:29] neg_lo:[1,0,0] neg_hi:[1,0,0]
	v_pk_fma_f32 v[102:103], v[102:103], v[102:103], s[28:29] neg_lo:[1,0,0] neg_hi:[1,0,0]
	v_exp_f32_e32 v96, v96
	v_exp_f32_e32 v97, v97
	v_exp_f32_e32 v98, v98
	v_exp_f32_e32 v99, v99
	v_exp_f32_e32 v100, v100
	v_exp_f32_e32 v101, v101
	v_exp_f32_e32 v102, v102
	v_exp_f32_e32 v103, v103
	v_pk_add_f32 v[104:105], v[28:29], v[12:13] neg_lo:[0,1] neg_hi:[0,1]
	v_pk_add_f32 v[106:107], v[28:29], v[14:15] neg_lo:[0,1] neg_hi:[0,1]
	v_pk_add_f32 v[108:109], v[26:27], v[10:11] op_sel:[1,0] op_sel_hi:[0,1] neg_lo:[0,1] neg_hi:[0,1]
	v_pk_add_f32 v[110:111], v[28:29], v[12:13] op_sel:[1,0] op_sel_hi:[0,1] neg_lo:[0,1] neg_hi:[0,1]
	v_pk_fma_f32 v[104:105], v[104:105], v[104:105], s[22:23] neg_lo:[1,0,0] neg_hi:[1,0,0]
	v_pk_fma_f32 v[106:107], v[106:107], v[106:107], s[28:29] neg_lo:[1,0,0] neg_hi:[1,0,0]
	v_pk_fma_f32 v[108:109], v[108:109], v[108:109], s[26:27] neg_lo:[1,0,0] neg_hi:[1,0,0]
	v_pk_fma_f32 v[110:111], v[110:111], v[110:111], s[26:27] neg_lo:[1,0,0] neg_hi:[1,0,0]
	v_exp_f32_e32 v104, v104
	v_exp_f32_e32 v105, v105
	v_exp_f32_e32 v106, v106
	v_exp_f32_e32 v107, v107
	v_exp_f32_e32 v108, v108
	v_exp_f32_e32 v109, v109
	v_exp_f32_e32 v110, v110
	v_exp_f32_e32 v111, v111
	v_pk_add_f32 v[72:73], s[30:31], v[96:97]
	v_pk_fma_f32 v[76:77], v[96:97], v[8:9], v[76:77]
	v_pk_add_f32 v[74:75], s[30:31], v[100:101]
	v_pk_add_f32 v[72:73], v[72:73], v[98:99]
	v_pk_fma_f32 v[76:77], v[98:99], v[10:11], v[76:77]
	v_pk_fma_f32 v[78:79], v[100:101], v[10:11], v[78:79]
	v_pk_add_f32 v[72:73], v[72:73], v[102:103]
	v_pk_fma_f32 v[76:77], v[102:103], v[12:13], v[76:77]
	v_pk_add_f32 v[96:97], v[26:27], v[16:17] neg_lo:[0,1] neg_hi:[0,1]
	v_pk_add_f32 v[98:99], v[24:25], v[18:19] neg_lo:[0,1] neg_hi:[0,1]
	v_pk_add_f32 v[100:101], v[26:27], v[18:19] neg_lo:[0,1] neg_hi:[0,1]
	v_pk_add_f32 v[102:103], v[28:29], v[18:19] neg_lo:[0,1] neg_hi:[0,1]
	v_pk_fma_f32 v[96:97], v[96:97], v[96:97], s[26:27] neg_lo:[1,0,0] neg_hi:[1,0,0]
	v_pk_fma_f32 v[98:99], v[98:99], v[98:99], s[26:27] neg_lo:[1,0,0] neg_hi:[1,0,0]
	v_pk_fma_f32 v[100:101], v[100:101], v[100:101], s[20:21] neg_lo:[1,0,0] neg_hi:[1,0,0]
	v_pk_fma_f32 v[102:103], v[102:103], v[102:103], s[26:27] neg_lo:[1,0,0] neg_hi:[1,0,0]
	v_exp_f32_e32 v96, v96
	v_exp_f32_e32 v97, v97
	v_exp_f32_e32 v98, v98
	v_exp_f32_e32 v99, v99
	v_exp_f32_e32 v100, v100
	v_exp_f32_e32 v101, v101
	v_exp_f32_e32 v102, v102
	v_exp_f32_e32 v103, v103
	v_pk_add_f32 v[74:75], v[74:75], v[104:105]
	v_pk_fma_f32 v[78:79], v[104:105], v[12:13], v[78:79]
	v_pk_add_f32 v[72:73], v[72:73], v[108:109] op_sel:[0,1] op_sel_hi:[1,0]
	v_pk_add_f32 v[74:75], v[74:75], v[106:107]
	v_pk_fma_f32 v[78:79], v[106:107], v[14:15], v[78:79]
	v_pk_fma_f32 v[76:77], v[108:109], v[10:11], v[76:77] op_sel:[1,1,0] op_sel_hi:[0,0,1]
	v_pk_add_f32 v[74:75], v[74:75], v[110:111] op_sel:[0,1] op_sel_hi:[1,0]
	v_pk_fma_f32 v[78:79], v[110:111], v[12:13], v[78:79] op_sel:[1,1,0] op_sel_hi:[0,0,1]
	v_pk_add_f32 v[104:105], v[26:27], v[20:21] neg_lo:[0,1] neg_hi:[0,1]
	v_pk_add_f32 v[106:107], v[28:29], v[20:21] neg_lo:[0,1] neg_hi:[0,1]
	v_pk_add_f32 v[108:109], v[30:31], v[20:21] neg_lo:[0,1] neg_hi:[0,1]
	v_pk_add_f32 v[110:111], v[28:29], v[22:23] neg_lo:[0,1] neg_hi:[0,1]
	v_pk_fma_f32 v[104:105], v[104:105], v[104:105], s[26:27] neg_lo:[1,0,0] neg_hi:[1,0,0]
	v_pk_fma_f32 v[106:107], v[106:107], v[106:107], s[20:21] neg_lo:[1,0,0] neg_hi:[1,0,0]
	v_pk_fma_f32 v[108:109], v[108:109], v[108:109], s[26:27] neg_lo:[1,0,0] neg_hi:[1,0,0]
	v_pk_fma_f32 v[110:111], v[110:111], v[110:111], s[26:27] neg_lo:[1,0,0] neg_hi:[1,0,0]
	v_exp_f32_e32 v104, v104
	v_exp_f32_e32 v105, v105
	v_exp_f32_e32 v106, v106
	v_exp_f32_e32 v107, v107
	v_exp_f32_e32 v108, v108
	v_exp_f32_e32 v109, v109
	v_exp_f32_e32 v110, v110
	v_exp_f32_e32 v111, v111
	v_pk_add_f32 v[72:73], v[72:73], v[96:97]
	v_pk_fma_f32 v[76:77], v[96:97], v[16:17], v[76:77]
	v_pk_add_f32 v[64:65], v[64:65], v[98:99]
	v_pk_fma_f32 v[68:69], v[98:99], v[24:25], v[68:69]
	v_pk_add_f32 v[72:73], v[72:73], v[100:101]
	v_pk_add_f32 v[64:65], v[64:65], v[100:101]
	v_pk_fma_f32 v[68:69], v[100:101], v[26:27], v[68:69]
	v_pk_fma_f32 v[76:77], v[100:101], v[18:19], v[76:77]
	v_pk_add_f32 v[64:65], v[64:65], v[102:103]
	v_pk_fma_f32 v[68:69], v[102:103], v[28:29], v[68:69]
	v_pk_add_f32 v[74:75], v[74:75], v[102:103]
	v_pk_fma_f32 v[78:79], v[102:103], v[18:19], v[78:79]
	v_pk_add_f32 v[96:97], v[26:27], v[18:19] op_sel:[1,0] op_sel_hi:[0,1] neg_lo:[0,1] neg_hi:[0,1]
	v_pk_add_f32 v[98:99], v[28:29], v[20:21] op_sel:[1,0] op_sel_hi:[0,1] neg_lo:[0,1] neg_hi:[0,1]
	v_pk_add_f32 v[100:101], v[26:27], v[24:25] neg_lo:[0,1] neg_hi:[0,1]
	v_pk_add_f32 v[102:103], v[28:29], v[26:27] neg_lo:[0,1] neg_hi:[0,1]
	v_pk_fma_f32 v[96:97], v[96:97], v[96:97], s[24:25] neg_lo:[1,0,0] neg_hi:[1,0,0]
	v_pk_fma_f32 v[98:99], v[98:99], v[98:99], s[24:25] neg_lo:[1,0,0] neg_hi:[1,0,0]
	v_pk_fma_f32 v[100:101], v[100:101], v[100:101], s[22:23] neg_lo:[1,0,0] neg_hi:[1,0,0]
	v_pk_fma_f32 v[102:103], v[102:103], v[102:103], s[22:23] neg_lo:[1,0,0] neg_hi:[1,0,0]
	v_exp_f32_e32 v96, v96
	v_exp_f32_e32 v97, v97
	v_exp_f32_e32 v98, v98
	v_exp_f32_e32 v99, v99
	v_exp_f32_e32 v100, v100
	v_exp_f32_e32 v101, v101
	v_exp_f32_e32 v102, v102
	v_exp_f32_e32 v103, v103
	v_pk_add_f32 v[66:67], v[66:67], v[104:105]
	v_pk_fma_f32 v[70:71], v[104:105], v[26:27], v[70:71]
	v_pk_add_f32 v[72:73], v[72:73], v[104:105]
	v_pk_fma_f32 v[76:77], v[104:105], v[20:21], v[76:77]
	v_pk_add_f32 v[66:67], v[66:67], v[106:107]
	v_pk_fma_f32 v[70:71], v[106:107], v[28:29], v[70:71]
	v_pk_add_f32 v[74:75], v[74:75], v[106:107]
	v_pk_fma_f32 v[78:79], v[106:107], v[20:21], v[78:79]
	v_pk_add_f32 v[66:67], v[66:67], v[108:109]
	v_pk_fma_f32 v[70:71], v[108:109], v[30:31], v[70:71]
	v_pk_add_f32 v[74:75], v[74:75], v[110:111]
	v_pk_fma_f32 v[78:79], v[110:111], v[22:23], v[78:79]
	v_pk_add_f32 v[104:105], v[30:31], v[28:29] neg_lo:[0,1] neg_hi:[0,1]
	v_pk_fma_f32 v[104:105], v[104:105], v[104:105], s[22:23] neg_lo:[1,0,0] neg_hi:[1,0,0]
	s_nop 0
	v_exp_f32_e32 v104, v104
	v_exp_f32_e64 v105, v105
	v_pk_add_f32 v[64:65], v[64:65], v[96:97]
	v_pk_fma_f32 v[68:69], v[96:97], v[26:27], v[68:69] op_sel:[0,1,0] op_sel_hi:[1,0,1]
	v_pk_add_f32 v[72:73], v[72:73], v[96:97] op_sel:[0,1] op_sel_hi:[1,0]
	v_pk_fma_f32 v[76:77], v[96:97], v[18:19], v[76:77] op_sel:[1,1,0] op_sel_hi:[0,0,1]
	v_pk_add_f32 v[66:67], v[66:67], v[98:99]
	v_pk_fma_f32 v[70:71], v[98:99], v[28:29], v[70:71] op_sel:[0,1,0] op_sel_hi:[1,0,1]
	v_pk_add_f32 v[74:75], v[74:75], v[98:99] op_sel:[0,1] op_sel_hi:[1,0]
	v_pk_fma_f32 v[78:79], v[98:99], v[20:21], v[78:79] op_sel:[1,1,0] op_sel_hi:[0,0,1]
	v_pk_add_f32 v[72:73], v[72:73], v[100:101]
	v_pk_fma_f32 v[76:77], v[100:101], v[24:25], v[76:77]
	v_pk_add_f32 v[74:75], v[74:75], v[102:103]
	v_pk_add_f32 v[72:73], v[72:73], v[102:103]
	v_pk_fma_f32 v[76:77], v[102:103], v[28:29], v[76:77]
	v_pk_fma_f32 v[78:79], v[102:103], v[26:27], v[78:79]
	s_nop 0
	v_sub_f32_e32 v96, v26, v9
	v_sub_f32_e32 v98, v28, v11
	v_sub_f32_e32 v100, v27, v12
	v_sub_f32_e32 v102, v29, v14
	v_sub_f32_e32 v97, v26, v17
	v_sub_f32_e32 v99, v25, v18
	v_sub_f32_e32 v101, v28, v19
	v_sub_f32_e64 v103, v27, v20
	v_fma_f32 v96, -v96, v96, s26
	v_fma_f32 v98, -v98, v98, s26
	v_fma_f32 v100, -v100, v100, s26
	v_fma_f32 v102, -v102, v102, s26
	v_fma_f32 v97, -v97, v97, s24
	v_fma_f32 v99, -v99, v99, s24
	v_fma_f32 v101, -v101, v101, s24
	v_fma_f32 v103, -v103, v103, s24
	v_exp_f32_e32 v96, v96
	v_exp_f32_e32 v98, v98
	v_exp_f32_e32 v100, v100
	v_exp_f32_e32 v102, v102
	v_exp_f32_e32 v97, v97
	v_exp_f32_e32 v99, v99
	v_exp_f32_e32 v101, v101
	v_exp_f32_e32 v103, v103
	v_pk_add_f32 v[74:75], v[74:75], v[104:105]
	v_pk_fma_f32 v[78:79], v[104:105], v[30:31], v[78:79]
	v_sub_f32_e32 v108, v30, v21
	v_sub_f32_e32 v110, v29, v22
	v_sub_f32_e32 v105, v26, v25
	v_sub_f32_e32 v104, v27, v26
	v_sub_f32_e32 v107, v28, v27
	v_sub_f32_e32 v106, v29, v28
	v_sub_f32_e64 v109, v30, v29
	v_fma_f32 v108, -v108, v108, s24
	v_fma_f32 v110, -v110, v110, s24
	v_fma_f32 v105, -v105, v105, s20
	v_fma_f32 v104, -v104, v104, s20
	v_fma_f32 v107, -v107, v107, s20
	v_fma_f32 v106, -v106, v106, s20
	v_fma_f32 v109, -v109, v109, s20
	v_exp_f32_e32 v108, v108
	v_exp_f32_e32 v110, v110
	v_exp_f32_e32 v105, v105
	v_exp_f32_e32 v104, v104
	v_exp_f32_e32 v107, v107
	v_exp_f32_e32 v106, v106
	v_exp_f32_e32 v109, v109
	v_add_f32_e32 v72, v72, v96
	v_fmac_f32_e32 v76, v96, v9
	v_add_f32_e32 v74, v74, v98
	v_fmac_f32_e32 v78, v98, v11
	v_add_f32_e32 v73, v73, v100
	v_fmac_f32_e32 v77, v100, v12
	v_add_f32_e32 v75, v75, v102
	v_fmac_f32_e32 v79, v102, v14
	v_add_f32_e32 v72, v72, v97
	v_fmac_f32_e32 v76, v97, v17
	v_add_f32_e32 v64, v64, v99
	v_fmac_f32_e32 v68, v99, v25
	v_add_f32_e32 v65, v65, v101
	v_fmac_f32_e32 v69, v101, v28
	v_add_f32_e32 v74, v74, v101
	v_fmac_f32_e32 v78, v101, v19
	v_add_f32_e32 v66, v66, v103
	v_fmac_f32_e32 v70, v103, v27
	v_add_f32_e32 v73, v73, v103
	v_fmac_f32_e32 v77, v103, v20
	v_add_f32_e32 v67, v67, v108
	v_fmac_f32_e32 v71, v108, v30
	v_add_f32_e32 v75, v75, v110
	v_fmac_f32_e32 v79, v110, v22
	v_add_f32_e32 v72, v72, v105
	v_fmac_f32_e32 v76, v105, v25
	v_add_f32_e32 v73, v73, v107
	v_fmac_f32_e32 v77, v107, v28
	v_add_f32_e32 v74, v74, v107
	v_fmac_f32_e32 v78, v107, v27
	v_add_f32_e32 v75, v75, v109
	v_fmac_f32_e64 v79, v109, v30
	v_pk_add_f32 v[72:73], v[72:73], v[104:105] op_sel_hi:[1,0]
	v_pk_fma_f32 v[76:77], v[104:105], v[26:27], v[76:77] op_sel:[0,1,0] op_sel_hi:[0,0,1]
	v_pk_add_f32 v[74:75], v[74:75], v[106:107] op_sel_hi:[1,0]
	v_pk_fma_f32 v[78:79], v[106:107], v[28:29], v[78:79] op_sel:[0,1,0] op_sel_hi:[0,0,1]
	s_waitcnt vmcnt(9)
	s_nop 0
	v_mov_b32_dpp v32, v36 row_shr:1 row_mask:0xf bank_mask:0xf
	v_mov_b32_dpp v33, v37 row_shr:1 row_mask:0xf bank_mask:0xf
	v_mov_b32_dpp v38, v34 row_shl:1 row_mask:0xf bank_mask:0xf
	v_mov_b32_dpp v39, v35 row_shl:1 row_mask:0xf bank_mask:0xf
	v_pk_mul_f32 v[34:35], v[34:35], s[32:33]
	v_pk_mul_f32 v[36:37], v[36:37], s[32:33]
	v_cndmask_b32_e64 v33, v33, v32, vcc
	v_cndmask_b32_e64 v38, v38, v39, s[16:17]
	v_pk_mul_f32 v[84:85], v[34:35], s[30:31]
	v_pk_mul_f32 v[86:87], v[36:37], s[30:31]
	v_pk_mul_f32 v[32:33], v[32:33], s[32:33]
	v_pk_mul_f32 v[38:39], v[38:39], s[32:33]
	v_pk_add_f32 v[96:97], v[34:35], v[16:17] neg_lo:[0,1] neg_hi:[0,1]
	v_pk_add_f32 v[98:99], v[32:33], v[18:19] neg_lo:[0,1] neg_hi:[0,1]
	v_pk_add_f32 v[100:101], v[34:35], v[18:19] neg_lo:[0,1] neg_hi:[0,1]
	v_pk_add_f32 v[102:103], v[36:37], v[18:19] neg_lo:[0,1] neg_hi:[0,1]
	v_pk_fma_f32 v[96:97], v[96:97], v[96:97], s[28:29] neg_lo:[1,0,0] neg_hi:[1,0,0]
	v_pk_fma_f32 v[98:99], v[98:99], v[98:99], s[28:29] neg_lo:[1,0,0] neg_hi:[1,0,0]
	v_pk_fma_f32 v[100:101], v[100:101], v[100:101], s[22:23] neg_lo:[1,0,0] neg_hi:[1,0,0]
	v_pk_fma_f32 v[102:103], v[102:103], v[102:103], s[28:29] neg_lo:[1,0,0] neg_hi:[1,0,0]
	v_exp_f32_e32 v96, v96
	v_exp_f32_e32 v97, v97
	v_exp_f32_e32 v98, v98
	v_exp_f32_e32 v99, v99
	v_exp_f32_e32 v100, v100
	v_exp_f32_e32 v101, v101
	v_exp_f32_e32 v102, v102
	v_exp_f32_e32 v103, v103
	v_pk_add_f32 v[104:105], v[34:35], v[20:21] neg_lo:[0,1] neg_hi:[0,1]
	v_pk_add_f32 v[106:107], v[36:37], v[20:21] neg_lo:[0,1] neg_hi:[0,1]
	v_pk_add_f32 v[108:109], v[38:39], v[20:21] neg_lo:[0,1] neg_hi:[0,1]
	v_pk_add_f32 v[110:111], v[36:37], v[22:23] neg_lo:[0,1] neg_hi:[0,1]
	v_pk_fma_f32 v[104:105], v[104:105], v[104:105], s[28:29] neg_lo:[1,0,0] neg_hi:[1,0,0]
	v_pk_fma_f32 v[106:107], v[106:107], v[106:107], s[22:23] neg_lo:[1,0,0] neg_hi:[1,0,0]
	v_pk_fma_f32 v[108:109], v[108:109], v[108:109], s[28:29] neg_lo:[1,0,0] neg_hi:[1,0,0]
	v_pk_fma_f32 v[110:111], v[110:111], v[110:111], s[28:29] neg_lo:[1,0,0] neg_hi:[1,0,0]
	v_exp_f32_e32 v104, v104
	v_exp_f32_e32 v105, v105
	v_exp_f32_e32 v106, v106
	v_exp_f32_e32 v107, v107
	v_exp_f32_e32 v108, v108
	v_exp_f32_e32 v109, v109
	v_exp_f32_e32 v110, v110
	v_exp_f32_e32 v111, v111
	v_pk_add_f32 v[80:81], s[30:31], v[96:97]
	v_pk_fma_f32 v[84:85], v[96:97], v[16:17], v[84:85]
	v_pk_add_f32 v[64:65], v[64:65], v[98:99]
	v_pk_fma_f32 v[68:69], v[98:99], v[32:33], v[68:69]
	v_pk_add_f32 v[80:81], v[80:81], v[100:101]
	v_pk_add_f32 v[64:65], v[64:65], v[100:101]
	v_pk_fma_f32 v[68:69], v[100:101], v[34:35], v[68:69]
	v_pk_fma_f32 v[84:85], v[100:101], v[18:19], v[84:85]
	v_pk_add_f32 v[64:65], v[64:65], v[102:103]
	v_pk_fma_f32 v[68:69], v[102:103], v[36:37], v[68:69]
	v_pk_add_f32 v[82:83], s[30:31], v[102:103]
	v_pk_fma_f32 v[86:87], v[102:103], v[18:19], v[86:87]
	v_pk_add_f32 v[96:97], v[34:35], v[18:19] op_sel:[1,0] op_sel_hi:[0,1] neg_lo:[0,1] neg_hi:[0,1]
	v_pk_add_f32 v[98:99], v[36:37], v[20:21] op_sel:[1,0] op_sel_hi:[0,1] neg_lo:[0,1] neg_hi:[0,1]
	v_pk_add_f32 v[100:101], v[34:35], v[24:25] neg_lo:[0,1] neg_hi:[0,1]
	v_pk_add_f32 v[102:103], v[32:33], v[26:27] neg_lo:[0,1] neg_hi:[0,1]
	v_pk_fma_f32 v[96:97], v[96:97], v[96:97], s[26:27] neg_lo:[1,0,0] neg_hi:[1,0,0]
	v_pk_fma_f32 v[98:99], v[98:99], v[98:99], s[26:27] neg_lo:[1,0,0] neg_hi:[1,0,0]
	v_pk_fma_f32 v[100:101], v[100:101], v[100:101], s[26:27] neg_lo:[1,0,0] neg_hi:[1,0,0]
	v_pk_fma_f32 v[102:103], v[102:103], v[102:103], s[26:27] neg_lo:[1,0,0] neg_hi:[1,0,0]
	v_exp_f32_e32 v96, v96
	v_exp_f32_e32 v97, v97
	v_exp_f32_e32 v98, v98
	v_exp_f32_e32 v99, v99
	v_exp_f32_e32 v100, v100
	v_exp_f32_e32 v101, v101
	v_exp_f32_e32 v102, v102
	v_exp_f32_e32 v103, v103
	v_pk_add_f32 v[66:67], v[66:67], v[104:105]
	v_pk_fma_f32 v[70:71], v[104:105], v[34:35], v[70:71]
	v_pk_add_f32 v[80:81], v[80:81], v[104:105]
	v_pk_fma_f32 v[84:85], v[104:105], v[20:21], v[84:85]
	v_pk_add_f32 v[66:67], v[66:67], v[106:107]
	v_pk_fma_f32 v[70:71], v[106:107], v[36:37], v[70:71]
	v_pk_add_f32 v[82:83], v[82:83], v[106:107]
	v_pk_fma_f32 v[86:87], v[106:107], v[20:21], v[86:87]
	v_pk_add_f32 v[66:67], v[66:67], v[108:109]
	v_pk_fma_f32 v[70:71], v[108:109], v[38:39], v[70:71]
	v_pk_add_f32 v[82:83], v[82:83], v[110:111]
	v_pk_fma_f32 v[86:87], v[110:111], v[22:23], v[86:87]
	v_pk_add_f32 v[104:105], v[34:35], v[26:27] neg_lo:[0,1] neg_hi:[0,1]
	v_pk_add_f32 v[106:107], v[36:37], v[26:27] neg_lo:[0,1] neg_hi:[0,1]
	v_pk_add_f32 v[108:109], v[34:35], v[28:29] neg_lo:[0,1] neg_hi:[0,1]
	v_pk_add_f32 v[110:111], v[36:37], v[28:29] neg_lo:[0,1] neg_hi:[0,1]
	v_pk_fma_f32 v[104:105], v[104:105], v[104:105], s[20:21] neg_lo:[1,0,0] neg_hi:[1,0,0]
	v_pk_fma_f32 v[106:107], v[106:107], v[106:107], s[26:27] neg_lo:[1,0,0] neg_hi:[1,0,0]
	v_pk_fma_f32 v[108:109], v[108:109], v[108:109], s[26:27] neg_lo:[1,0,0] neg_hi:[1,0,0]
	v_pk_fma_f32 v[110:111], v[110:111], v[110:111], s[20:21] neg_lo:[1,0,0] neg_hi:[1,0,0]
	v_exp_f32_e32 v104, v104
	v_exp_f32_e32 v105, v105
	v_exp_f32_e32 v106, v106
	v_exp_f32_e32 v107, v107
	v_exp_f32_e32 v108, v108
	v_exp_f32_e32 v109, v109
	v_exp_f32_e32 v110, v110
	v_exp_f32_e32 v111, v111
	v_pk_add_f32 v[64:65], v[64:65], v[96:97]
	v_pk_fma_f32 v[68:69], v[96:97], v[34:35], v[68:69] op_sel:[0,1,0] op_sel_hi:[1,0,1]
	v_pk_add_f32 v[80:81], v[80:81], v[96:97] op_sel:[0,1] op_sel_hi:[1,0]
	v_pk_fma_f32 v[84:85], v[96:97], v[18:19], v[84:85] op_sel:[1,1,0] op_sel_hi:[0,0,1]
	v_pk_add_f32 v[66:67], v[66:67], v[98:99]
	v_pk_fma_f32 v[70:71], v[98:99], v[36:37], v[70:71] op_sel:[0,1,0] op_sel_hi:[1,0,1]
	v_pk_add_f32 v[82:83], v[82:83], v[98:99] op_sel:[0,1] op_sel_hi:[1,0]
	v_pk_fma_f32 v[86:87], v[98:99], v[20:21], v[86:87] op_sel:[1,1,0] op_sel_hi:[0,0,1]
	v_pk_add_f32 v[80:81], v[80:81], v[100:101]
	v_pk_fma_f32 v[84:85], v[100:101], v[24:25], v[84:85]
	v_pk_add_f32 v[72:73], v[72:73], v[102:103]
	v_pk_fma_f32 v[76:77], v[102:103], v[32:33], v[76:77]
	v_pk_add_f32 v[96:97], v[38:39], v[28:29] neg_lo:[0,1] neg_hi:[0,1]
	v_pk_add_f32 v[98:99], v[36:37], v[30:31] neg_lo:[0,1] neg_hi:[0,1]
	v_pk_add_f32 v[100:101], v[34:35], v[26:27] op_sel:[1,0] op_sel_hi:[0,1] neg_lo:[0,1] neg_hi:[0,1]
	v_pk_add_f32 v[102:103], v[36:37], v[28:29] op_sel:[1,0] op_sel_hi:[0,1] neg_lo:[0,1] neg_hi:[0,1]
	v_pk_fma_f32 v[96:97], v[96:97], v[96:97], s[26:27] neg_lo:[1,0,0] neg_hi:[1,0,0]
	v_pk_fma_f32 v[98:99], v[98:99], v[98:99], s[26:27] neg_lo:[1,0,0] neg_hi:[1,0,0]
	v_pk_fma_f32 v[100:101], v[100:101], v[100:101], s[24:25] neg_lo:[1,0,0] neg_hi:[1,0,0]
	v_pk_fma_f32 v[102:103], v[102:103], v[102:103], s[24:25] neg_lo:[1,0,0] neg_hi:[1,0,0]
	v_exp_f32_e32 v96, v96
	v_exp_f32_e32 v97, v97
	v_exp_f32_e32 v98, v98
	v_exp_f32_e32 v99, v99
	v_exp_f32_e32 v100, v100
	v_exp_f32_e32 v101, v101
	v_exp_f32_e32 v102, v102
	v_exp_f32_e32 v103, v103
	v_pk_add_f32 v[72:73], v[72:73], v[104:105]
	v_pk_fma_f32 v[76:77], v[104:105], v[34:35], v[76:77]
	v_pk_add_f32 v[80:81], v[80:81], v[104:105]
	v_pk_fma_f32 v[84:85], v[104:105], v[26:27], v[84:85]
	v_pk_add_f32 v[72:73], v[72:73], v[106:107]
	v_pk_fma_f32 v[76:77], v[106:107], v[36:37], v[76:77]
	v_pk_add_f32 v[82:83], v[82:83], v[106:107]
	v_pk_fma_f32 v[86:87], v[106:107], v[26:27], v[86:87]
	v_pk_add_f32 v[74:75], v[74:75], v[108:109]
	v_pk_fma_f32 v[78:79], v[108:109], v[34:35], v[78:79]
	v_pk_add_f32 v[80:81], v[80:81], v[108:109]
	v_pk_fma_f32 v[84:85], v[108:109], v[28:29], v[84:85]
	v_pk_add_f32 v[74:75], v[74:75], v[110:111]
	v_pk_fma_f32 v[78:79], v[110:111], v[36:37], v[78:79]
	v_pk_add_f32 v[82:83], v[82:83], v[110:111]
	v_pk_fma_f32 v[86:87], v[110:111], v[28:29], v[86:87]
	v_pk_add_f32 v[104:105], v[34:35], v[32:33] neg_lo:[0,1] neg_hi:[0,1]
	v_pk_add_f32 v[106:107], v[36:37], v[34:35] neg_lo:[0,1] neg_hi:[0,1]
	v_pk_add_f32 v[108:109], v[38:39], v[36:37] neg_lo:[0,1] neg_hi:[0,1]
	v_pk_fma_f32 v[104:105], v[104:105], v[104:105], s[22:23] neg_lo:[1,0,0] neg_hi:[1,0,0]
	v_pk_fma_f32 v[106:107], v[106:107], v[106:107], s[22:23] neg_lo:[1,0,0] neg_hi:[1,0,0]
	v_pk_fma_f32 v[108:109], v[108:109], v[108:109], s[22:23] neg_lo:[1,0,0] neg_hi:[1,0,0]
	v_exp_f32_e32 v104, v104
	v_exp_f32_e32 v105, v105
	v_exp_f32_e32 v106, v106
	v_exp_f32_e32 v107, v107
	v_exp_f32_e32 v108, v108
	v_exp_f32_e32 v109, v109
	v_pk_add_f32 v[74:75], v[74:75], v[96:97]
	v_pk_fma_f32 v[78:79], v[96:97], v[38:39], v[78:79]
	v_pk_add_f32 v[82:83], v[82:83], v[98:99]
	v_pk_fma_f32 v[86:87], v[98:99], v[30:31], v[86:87]
	v_pk_add_f32 v[72:73], v[72:73], v[100:101]
	v_pk_fma_f32 v[76:77], v[100:101], v[34:35], v[76:77] op_sel:[0,1,0] op_sel_hi:[1,0,1]
	v_pk_add_f32 v[80:81], v[80:81], v[100:101] op_sel:[0,1] op_sel_hi:[1,0]
	v_pk_fma_f32 v[84:85], v[100:101], v[26:27], v[84:85] op_sel:[1,1,0] op_sel_hi:[0,0,1]
	v_pk_add_f32 v[74:75], v[74:75], v[102:103]
	v_pk_fma_f32 v[78:79], v[102:103], v[36:37], v[78:79] op_sel:[0,1,0] op_sel_hi:[1,0,1]
	v_pk_add_f32 v[82:83], v[82:83], v[102:103] op_sel:[0,1] op_sel_hi:[1,0]
	v_pk_fma_f32 v[86:87], v[102:103], v[28:29], v[86:87] op_sel:[1,1,0] op_sel_hi:[0,0,1]
	v_sub_f32_e32 v96, v34, v17
	v_sub_f32_e32 v98, v33, v18
	v_sub_f32_e32 v100, v36, v19
	v_sub_f32_e32 v102, v35, v20
	v_sub_f32_e32 v97, v38, v21
	v_sub_f32_e32 v99, v37, v22
	v_sub_f32_e32 v101, v34, v25
	v_sub_f32_e32 v103, v33, v26
	v_fma_f32 v96, -v96, v96, s26
	v_fma_f32 v98, -v98, v98, s26
	v_fma_f32 v100, -v100, v100, s26
	v_fma_f32 v102, -v102, v102, s26
	v_fma_f32 v97, -v97, v97, s26
	v_fma_f32 v99, -v99, v99, s26
	v_fma_f32 v101, -v101, v101, s24
	v_fma_f32 v103, -v103, v103, s24
	v_exp_f32_e32 v96, v96
	v_exp_f32_e32 v98, v98
	v_exp_f32_e32 v100, v100
	v_exp_f32_e32 v102, v102
	v_exp_f32_e32 v97, v97
	v_exp_f32_e32 v99, v99
	v_exp_f32_e32 v101, v101
	v_exp_f32_e32 v103, v103
	v_pk_add_f32 v[80:81], v[80:81], v[104:105]
	v_pk_fma_f32 v[84:85], v[104:105], v[32:33], v[84:85]
	v_pk_add_f32 v[82:83], v[82:83], v[106:107]
	v_pk_add_f32 v[80:81], v[80:81], v[106:107]
	v_pk_fma_f32 v[84:85], v[106:107], v[36:37], v[84:85]
	v_pk_fma_f32 v[86:87], v[106:107], v[34:35], v[86:87]
	v_pk_add_f32 v[82:83], v[82:83], v[108:109]
	v_pk_fma_f32 v[86:87], v[108:109], v[38:39], v[86:87]
	v_sub_f32_e32 v108, v36, v27
	v_sub_f32_e32 v110, v35, v28
	v_sub_f32_e32 v105, v38, v29
	v_sub_f32_e32 v107, v37, v30
	v_sub_f32_e32 v109, v34, v33
	v_sub_f32_e32 v104, v35, v34
	v_sub_f32_e32 v111, v36, v35
	v_sub_f32_e32 v106, v37, v36
	v_fma_f32 v108, -v108, v108, s24
	v_fma_f32 v110, -v110, v110, s24
	v_fma_f32 v105, -v105, v105, s24
	v_fma_f32 v107, -v107, v107, s24
	v_fma_f32 v109, -v109, v109, s20
	v_fma_f32 v104, -v104, v104, s20
	v_fma_f32 v111, -v111, v111, s20
	v_fma_f32 v106, -v106, v106, s20
	v_exp_f32_e32 v108, v108
	v_exp_f32_e32 v110, v110
	v_exp_f32_e32 v105, v105
	v_exp_f32_e32 v107, v107
	v_exp_f32_e32 v109, v109
	v_exp_f32_e32 v104, v104
	v_exp_f32_e32 v111, v111
	v_exp_f32_e32 v106, v106
	v_add_f32_e32 v80, v80, v96
	v_fmac_f32_e32 v84, v96, v17
	v_add_f32_e32 v64, v64, v98
	v_fmac_f32_e32 v68, v98, v33
	v_add_f32_e32 v65, v65, v100
	v_fmac_f32_e32 v69, v100, v36
	v_add_f32_e32 v82, v82, v100
	v_fmac_f32_e32 v86, v100, v19
	v_add_f32_e32 v66, v66, v102
	v_fmac_f32_e32 v70, v102, v35
	v_add_f32_e32 v81, v81, v102
	v_fmac_f32_e32 v85, v102, v20
	v_add_f32_e32 v67, v67, v97
	v_fmac_f32_e32 v71, v97, v38
	v_add_f32_e32 v83, v83, v99
	v_fmac_f32_e32 v87, v99, v22
	v_add_f32_e32 v80, v80, v101
	v_fmac_f32_e32 v84, v101, v25
	v_add_f32_e32 v72, v72, v103
	v_fmac_f32_e32 v76, v103, v33
	v_sub_f32_e64 v96, v38, v37
	v_fma_f32 v96, -v96, v96, s20
	s_nop 0
	v_exp_f32_e32 v96, v96
	v_add_f32_e32 v73, v73, v108
	v_fmac_f32_e32 v77, v108, v36
	v_add_f32_e32 v82, v82, v108
	v_fmac_f32_e32 v86, v108, v27
	v_add_f32_e32 v74, v74, v110
	v_fmac_f32_e32 v78, v110, v35
	v_add_f32_e32 v81, v81, v110
	v_fmac_f32_e32 v85, v110, v28
	v_add_f32_e32 v75, v75, v105
	v_fmac_f32_e32 v79, v105, v38
	v_add_f32_e32 v83, v83, v107
	v_fmac_f32_e32 v87, v107, v30
	v_add_f32_e32 v80, v80, v109
	v_fmac_f32_e32 v84, v109, v33
	v_add_f32_e32 v81, v81, v111
	v_fmac_f32_e32 v85, v111, v36
	v_add_f32_e32 v82, v82, v111
	v_fmac_f32_e32 v86, v111, v35
	v_pk_add_f32 v[80:81], v[80:81], v[104:105] op_sel_hi:[1,0]
	v_pk_fma_f32 v[84:85], v[104:105], v[34:35], v[84:85] op_sel:[0,1,0] op_sel_hi:[0,0,1]
	v_pk_add_f32 v[82:83], v[82:83], v[106:107] op_sel_hi:[1,0]
	v_pk_fma_f32 v[86:87], v[106:107], v[36:37], v[86:87] op_sel:[0,1,0] op_sel_hi:[0,0,1]
	s_nop 0
	v_add_f32_e32 v83, v83, v96
	v_fmac_f32_e32 v87, v96, v38
	v_rcp_f32_e32 v96, v64
	v_rcp_f32_e32 v97, v65
	v_rcp_f32_e32 v98, v66
	v_rcp_f32_e64 v99, v67
	v_pk_mul_f32 v[68:69], v[68:69], s[34:35]
	v_pk_mul_f32 v[70:71], v[70:71], s[34:35]
	v_pk_mul_f32 v[68:69], v[68:69], v[96:97]
	v_pk_mul_f32 v[70:71], v[70:71], v[98:99]
	buffer_store_dwordx4 v[68:71], v114, s[12:15], 0 offen sc1
	s_waitcnt vmcnt(7)
	s_nop 0
	v_mov_b32_dpp v40, v44 row_shr:1 row_mask:0xf bank_mask:0xf
	v_mov_b32_dpp v41, v45 row_shr:1 row_mask:0xf bank_mask:0xf
	v_mov_b32_dpp v46, v42 row_shl:1 row_mask:0xf bank_mask:0xf
	v_mov_b32_dpp v47, v43 row_shl:1 row_mask:0xf bank_mask:0xf
	v_pk_mul_f32 v[42:43], v[42:43], s[32:33]
	v_pk_mul_f32 v[44:45], v[44:45], s[32:33]
	v_cndmask_b32_e64 v41, v41, v40, vcc
	v_cndmask_b32_e64 v46, v46, v47, s[16:17]
	v_pk_mul_f32 v[92:93], v[42:43], s[30:31]
	v_pk_mul_f32 v[94:95], v[44:45], s[30:31]
	v_pk_mul_f32 v[40:41], v[40:41], s[32:33]
	v_pk_mul_f32 v[46:47], v[46:47], s[32:33]
	v_pk_add_f32 v[96:97], v[42:43], v[24:25] neg_lo:[0,1] neg_hi:[0,1]
	v_pk_add_f32 v[98:99], v[40:41], v[26:27] neg_lo:[0,1] neg_hi:[0,1]
	v_pk_add_f32 v[100:101], v[42:43], v[26:27] neg_lo:[0,1] neg_hi:[0,1]
	v_pk_add_f32 v[102:103], v[44:45], v[26:27] neg_lo:[0,1] neg_hi:[0,1]
	v_pk_fma_f32 v[96:97], v[96:97], v[96:97], s[28:29] neg_lo:[1,0,0] neg_hi:[1,0,0]
	v_pk_fma_f32 v[98:99], v[98:99], v[98:99], s[28:29] neg_lo:[1,0,0] neg_hi:[1,0,0]
	v_pk_fma_f32 v[100:101], v[100:101], v[100:101], s[22:23] neg_lo:[1,0,0] neg_hi:[1,0,0]
	v_pk_fma_f32 v[102:103], v[102:103], v[102:103], s[28:29] neg_lo:[1,0,0] neg_hi:[1,0,0]
	v_exp_f32_e32 v96, v96
	v_exp_f32_e32 v97, v97
	v_exp_f32_e32 v98, v98
	v_exp_f32_e32 v99, v99
	v_exp_f32_e32 v100, v100
	v_exp_f32_e32 v101, v101
	v_exp_f32_e32 v102, v102
	v_exp_f32_e32 v103, v103
	v_pk_add_f32 v[104:105], v[42:43], v[28:29] neg_lo:[0,1] neg_hi:[0,1]
	v_pk_add_f32 v[106:107], v[44:45], v[28:29] neg_lo:[0,1] neg_hi:[0,1]
	v_pk_add_f32 v[108:109], v[46:47], v[28:29] neg_lo:[0,1] neg_hi:[0,1]
	v_pk_add_f32 v[110:111], v[44:45], v[30:31] neg_lo:[0,1] neg_hi:[0,1]
	v_pk_fma_f32 v[104:105], v[104:105], v[104:105], s[28:29] neg_lo:[1,0,0] neg_hi:[1,0,0]
	v_pk_fma_f32 v[106:107], v[106:107], v[106:107], s[22:23] neg_lo:[1,0,0] neg_hi:[1,0,0]
	v_pk_fma_f32 v[108:109], v[108:109], v[108:109], s[28:29] neg_lo:[1,0,0] neg_hi:[1,0,0]
	v_pk_fma_f32 v[110:111], v[110:111], v[110:111], s[28:29] neg_lo:[1,0,0] neg_hi:[1,0,0]
	v_exp_f32_e32 v104, v104
	v_exp_f32_e32 v105, v105
	v_exp_f32_e32 v106, v106
	v_exp_f32_e32 v107, v107
	v_exp_f32_e32 v108, v108
	v_exp_f32_e32 v109, v109
	v_exp_f32_e32 v110, v110
	v_exp_f32_e32 v111, v111
	v_pk_add_f32 v[88:89], s[30:31], v[96:97]
	v_pk_fma_f32 v[92:93], v[96:97], v[24:25], v[92:93]
	v_pk_add_f32 v[72:73], v[72:73], v[98:99]
	v_pk_fma_f32 v[76:77], v[98:99], v[40:41], v[76:77]
	v_pk_add_f32 v[88:89], v[88:89], v[100:101]
	v_pk_add_f32 v[72:73], v[72:73], v[100:101]
	v_pk_fma_f32 v[76:77], v[100:101], v[42:43], v[76:77]
	v_pk_fma_f32 v[92:93], v[100:101], v[26:27], v[92:93]
	v_pk_add_f32 v[72:73], v[72:73], v[102:103]
	v_pk_fma_f32 v[76:77], v[102:103], v[44:45], v[76:77]
	v_pk_add_f32 v[90:91], s[30:31], v[102:103]
	v_pk_fma_f32 v[94:95], v[102:103], v[26:27], v[94:95]
	v_pk_add_f32 v[96:97], v[42:43], v[26:27] op_sel:[1,0] op_sel_hi:[0,1] neg_lo:[0,1] neg_hi:[0,1]
	v_pk_add_f32 v[98:99], v[44:45], v[28:29] op_sel:[1,0] op_sel_hi:[0,1] neg_lo:[0,1] neg_hi:[0,1]
	v_pk_add_f32 v[100:101], v[42:43], v[32:33] neg_lo:[0,1] neg_hi:[0,1]
	v_pk_add_f32 v[102:103], v[40:41], v[34:35] neg_lo:[0,1] neg_hi:[0,1]
	v_pk_fma_f32 v[96:97], v[96:97], v[96:97], s[26:27] neg_lo:[1,0,0] neg_hi:[1,0,0]
	v_pk_fma_f32 v[98:99], v[98:99], v[98:99], s[26:27] neg_lo:[1,0,0] neg_hi:[1,0,0]
	v_pk_fma_f32 v[100:101], v[100:101], v[100:101], s[26:27] neg_lo:[1,0,0] neg_hi:[1,0,0]
	v_pk_fma_f32 v[102:103], v[102:103], v[102:103], s[26:27] neg_lo:[1,0,0] neg_hi:[1,0,0]
	v_exp_f32_e32 v96, v96
	v_exp_f32_e32 v97, v97
	v_exp_f32_e32 v98, v98
	v_exp_f32_e32 v99, v99
	v_exp_f32_e32 v100, v100
	v_exp_f32_e32 v101, v101
	v_exp_f32_e32 v102, v102
	v_exp_f32_e32 v103, v103
	v_pk_add_f32 v[74:75], v[74:75], v[104:105]
	v_pk_fma_f32 v[78:79], v[104:105], v[42:43], v[78:79]
	v_pk_add_f32 v[88:89], v[88:89], v[104:105]
	v_pk_fma_f32 v[92:93], v[104:105], v[28:29], v[92:93]
	v_pk_add_f32 v[74:75], v[74:75], v[106:107]
	v_pk_fma_f32 v[78:79], v[106:107], v[44:45], v[78:79]
	v_pk_add_f32 v[90:91], v[90:91], v[106:107]
	v_pk_fma_f32 v[94:95], v[106:107], v[28:29], v[94:95]
	v_pk_add_f32 v[74:75], v[74:75], v[108:109]
	v_pk_fma_f32 v[78:79], v[108:109], v[46:47], v[78:79]
	v_pk_add_f32 v[90:91], v[90:91], v[110:111]
	v_pk_fma_f32 v[94:95], v[110:111], v[30:31], v[94:95]
	v_pk_add_f32 v[104:105], v[42:43], v[34:35] neg_lo:[0,1] neg_hi:[0,1]
	v_pk_add_f32 v[106:107], v[44:45], v[34:35] neg_lo:[0,1] neg_hi:[0,1]
	v_pk_add_f32 v[108:109], v[42:43], v[36:37] neg_lo:[0,1] neg_hi:[0,1]
	v_pk_add_f32 v[110:111], v[44:45], v[36:37] neg_lo:[0,1] neg_hi:[0,1]
	v_pk_fma_f32 v[104:105], v[104:105], v[104:105], s[20:21] neg_lo:[1,0,0] neg_hi:[1,0,0]
	v_pk_fma_f32 v[106:107], v[106:107], v[106:107], s[26:27] neg_lo:[1,0,0] neg_hi:[1,0,0]
	v_pk_fma_f32 v[108:109], v[108:109], v[108:109], s[26:27] neg_lo:[1,0,0] neg_hi:[1,0,0]
	v_pk_fma_f32 v[110:111], v[110:111], v[110:111], s[20:21] neg_lo:[1,0,0] neg_hi:[1,0,0]
	v_exp_f32_e32 v104, v104
	v_exp_f32_e32 v105, v105
	v_exp_f32_e32 v106, v106
	v_exp_f32_e32 v107, v107
	v_exp_f32_e32 v108, v108
	v_exp_f32_e32 v109, v109
	v_exp_f32_e32 v110, v110
	v_exp_f32_e32 v111, v111
	v_pk_add_f32 v[72:73], v[72:73], v[96:97]
	v_pk_fma_f32 v[76:77], v[96:97], v[42:43], v[76:77] op_sel:[0,1,0] op_sel_hi:[1,0,1]
	v_pk_add_f32 v[88:89], v[88:89], v[96:97] op_sel:[0,1] op_sel_hi:[1,0]
	v_pk_fma_f32 v[92:93], v[96:97], v[26:27], v[92:93] op_sel:[1,1,0] op_sel_hi:[0,0,1]
	v_pk_add_f32 v[74:75], v[74:75], v[98:99]
	v_pk_fma_f32 v[78:79], v[98:99], v[44:45], v[78:79] op_sel:[0,1,0] op_sel_hi:[1,0,1]
	v_pk_add_f32 v[90:91], v[90:91], v[98:99] op_sel:[0,1] op_sel_hi:[1,0]
	v_pk_fma_f32 v[94:95], v[98:99], v[28:29], v[94:95] op_sel:[1,1,0] op_sel_hi:[0,0,1]
	v_pk_add_f32 v[88:89], v[88:89], v[100:101]
	v_pk_fma_f32 v[92:93], v[100:101], v[32:33], v[92:93]
	v_pk_add_f32 v[80:81], v[80:81], v[102:103]
	v_pk_fma_f32 v[84:85], v[102:103], v[40:41], v[84:85]
	v_pk_add_f32 v[96:97], v[46:47], v[36:37] neg_lo:[0,1] neg_hi:[0,1]
	v_pk_add_f32 v[98:99], v[44:45], v[38:39] neg_lo:[0,1] neg_hi:[0,1]
	v_pk_add_f32 v[100:101], v[42:43], v[34:35] op_sel:[1,0] op_sel_hi:[0,1] neg_lo:[0,1] neg_hi:[0,1]
	v_pk_add_f32 v[102:103], v[44:45], v[36:37] op_sel:[1,0] op_sel_hi:[0,1] neg_lo:[0,1] neg_hi:[0,1]
	v_pk_fma_f32 v[96:97], v[96:97], v[96:97], s[26:27] neg_lo:[1,0,0] neg_hi:[1,0,0]
	v_pk_fma_f32 v[98:99], v[98:99], v[98:99], s[26:27] neg_lo:[1,0,0] neg_hi:[1,0,0]
	v_pk_fma_f32 v[100:101], v[100:101], v[100:101], s[24:25] neg_lo:[1,0,0] neg_hi:[1,0,0]
	v_pk_fma_f32 v[102:103], v[102:103], v[102:103], s[24:25] neg_lo:[1,0,0] neg_hi:[1,0,0]
	v_exp_f32_e32 v96, v96
	v_exp_f32_e32 v97, v97
	v_exp_f32_e32 v98, v98
	v_exp_f32_e32 v99, v99
	v_exp_f32_e32 v100, v100
	v_exp_f32_e32 v101, v101
	v_exp_f32_e32 v102, v102
	v_exp_f32_e32 v103, v103
	v_pk_add_f32 v[80:81], v[80:81], v[104:105]
	v_pk_fma_f32 v[84:85], v[104:105], v[42:43], v[84:85]
	v_pk_add_f32 v[88:89], v[88:89], v[104:105]
	v_pk_fma_f32 v[92:93], v[104:105], v[34:35], v[92:93]
	v_pk_add_f32 v[80:81], v[80:81], v[106:107]
	v_pk_fma_f32 v[84:85], v[106:107], v[44:45], v[84:85]
	v_pk_add_f32 v[90:91], v[90:91], v[106:107]
	v_pk_fma_f32 v[94:95], v[106:107], v[34:35], v[94:95]
	v_pk_add_f32 v[82:83], v[82:83], v[108:109]
	v_pk_fma_f32 v[86:87], v[108:109], v[42:43], v[86:87]
	v_pk_add_f32 v[88:89], v[88:89], v[108:109]
	v_pk_fma_f32 v[92:93], v[108:109], v[36:37], v[92:93]
	v_pk_add_f32 v[82:83], v[82:83], v[110:111]
	v_pk_fma_f32 v[86:87], v[110:111], v[44:45], v[86:87]
	v_pk_add_f32 v[90:91], v[90:91], v[110:111]
	v_pk_fma_f32 v[94:95], v[110:111], v[36:37], v[94:95]
	v_pk_add_f32 v[104:105], v[42:43], v[40:41] neg_lo:[0,1] neg_hi:[0,1]
	v_pk_add_f32 v[106:107], v[44:45], v[42:43] neg_lo:[0,1] neg_hi:[0,1]
	v_pk_add_f32 v[108:109], v[46:47], v[44:45] neg_lo:[0,1] neg_hi:[0,1]
	v_pk_fma_f32 v[104:105], v[104:105], v[104:105], s[22:23] neg_lo:[1,0,0] neg_hi:[1,0,0]
	v_pk_fma_f32 v[106:107], v[106:107], v[106:107], s[22:23] neg_lo:[1,0,0] neg_hi:[1,0,0]
	v_pk_fma_f32 v[108:109], v[108:109], v[108:109], s[22:23] neg_lo:[1,0,0] neg_hi:[1,0,0]
	v_exp_f32_e32 v104, v104
	v_exp_f32_e32 v105, v105
	v_exp_f32_e32 v106, v106
	v_exp_f32_e32 v107, v107
	v_exp_f32_e32 v108, v108
	v_exp_f32_e32 v109, v109
	v_pk_add_f32 v[82:83], v[82:83], v[96:97]
	v_pk_fma_f32 v[86:87], v[96:97], v[46:47], v[86:87]
	v_pk_add_f32 v[90:91], v[90:91], v[98:99]
	v_pk_fma_f32 v[94:95], v[98:99], v[38:39], v[94:95]
	v_pk_add_f32 v[80:81], v[80:81], v[100:101]
	v_pk_fma_f32 v[84:85], v[100:101], v[42:43], v[84:85] op_sel:[0,1,0] op_sel_hi:[1,0,1]
	v_pk_add_f32 v[88:89], v[88:89], v[100:101] op_sel:[0,1] op_sel_hi:[1,0]
	v_pk_fma_f32 v[92:93], v[100:101], v[34:35], v[92:93] op_sel:[1,1,0] op_sel_hi:[0,0,1]
	v_pk_add_f32 v[82:83], v[82:83], v[102:103]
	v_pk_fma_f32 v[86:87], v[102:103], v[44:45], v[86:87] op_sel:[0,1,0] op_sel_hi:[1,0,1]
	v_pk_add_f32 v[90:91], v[90:91], v[102:103] op_sel:[0,1] op_sel_hi:[1,0]
	v_pk_fma_f32 v[94:95], v[102:103], v[36:37], v[94:95] op_sel:[1,1,0] op_sel_hi:[0,0,1]
	v_sub_f32_e32 v96, v42, v25
	v_sub_f32_e32 v98, v41, v26
	v_sub_f32_e32 v100, v44, v27
	v_sub_f32_e32 v102, v43, v28
	v_sub_f32_e32 v97, v46, v29
	v_sub_f32_e32 v99, v45, v30
	v_sub_f32_e32 v101, v42, v33
	v_sub_f32_e32 v103, v41, v34
	v_fma_f32 v96, -v96, v96, s26
	v_fma_f32 v98, -v98, v98, s26
	v_fma_f32 v100, -v100, v100, s26
	v_fma_f32 v102, -v102, v102, s26
	v_fma_f32 v97, -v97, v97, s26
	v_fma_f32 v99, -v99, v99, s26
	v_fma_f32 v101, -v101, v101, s24
	v_fma_f32 v103, -v103, v103, s24
	v_exp_f32_e32 v96, v96
	v_exp_f32_e32 v98, v98
	v_exp_f32_e32 v100, v100
	v_exp_f32_e32 v102, v102
	v_exp_f32_e32 v97, v97
	v_exp_f32_e32 v99, v99
	v_exp_f32_e32 v101, v101
	v_exp_f32_e32 v103, v103
	v_pk_add_f32 v[88:89], v[88:89], v[104:105]
	v_pk_fma_f32 v[92:93], v[104:105], v[40:41], v[92:93]
	v_pk_add_f32 v[90:91], v[90:91], v[106:107]
	v_pk_add_f32 v[88:89], v[88:89], v[106:107]
	v_pk_fma_f32 v[92:93], v[106:107], v[44:45], v[92:93]
	v_pk_fma_f32 v[94:95], v[106:107], v[42:43], v[94:95]
	v_pk_add_f32 v[90:91], v[90:91], v[108:109]
	v_pk_fma_f32 v[94:95], v[108:109], v[46:47], v[94:95]
	v_sub_f32_e32 v108, v44, v35
	v_sub_f32_e32 v110, v43, v36
	v_sub_f32_e32 v105, v46, v37
	v_sub_f32_e32 v107, v45, v38
	v_sub_f32_e32 v109, v42, v41
	v_sub_f32_e32 v104, v43, v42
	v_sub_f32_e32 v111, v44, v43
	v_sub_f32_e32 v106, v45, v44
	v_fma_f32 v108, -v108, v108, s24
	v_fma_f32 v110, -v110, v110, s24
	v_fma_f32 v105, -v105, v105, s24
	v_fma_f32 v107, -v107, v107, s24
	v_fma_f32 v109, -v109, v109, s20
	v_fma_f32 v104, -v104, v104, s20
	v_fma_f32 v111, -v111, v111, s20
	v_fma_f32 v106, -v106, v106, s20
	v_exp_f32_e32 v108, v108
	v_exp_f32_e32 v110, v110
	v_exp_f32_e32 v105, v105
	v_exp_f32_e32 v107, v107
	v_exp_f32_e32 v109, v109
	v_exp_f32_e32 v104, v104
	v_exp_f32_e32 v111, v111
	v_exp_f32_e32 v106, v106
	v_add_f32_e32 v88, v88, v96
	v_fmac_f32_e32 v92, v96, v25
	v_add_f32_e32 v72, v72, v98
	v_fmac_f32_e32 v76, v98, v41
	v_add_f32_e32 v73, v73, v100
	v_fmac_f32_e32 v77, v100, v44
	v_add_f32_e32 v90, v90, v100
	v_fmac_f32_e32 v94, v100, v27
	v_add_f32_e32 v74, v74, v102
	v_fmac_f32_e32 v78, v102, v43
	v_add_f32_e32 v89, v89, v102
	v_fmac_f32_e32 v93, v102, v28
	v_add_f32_e32 v75, v75, v97
	v_fmac_f32_e32 v79, v97, v46
	v_add_f32_e32 v91, v91, v99
	v_fmac_f32_e32 v95, v99, v30
	v_add_f32_e32 v88, v88, v101
	v_fmac_f32_e32 v92, v101, v33
	v_add_f32_e32 v80, v80, v103
	v_fmac_f32_e32 v84, v103, v41
	v_sub_f32_e64 v96, v46, v45
	v_fma_f32 v96, -v96, v96, s20
	s_nop 0
	v_exp_f32_e32 v96, v96
	v_add_f32_e32 v81, v81, v108
	v_fmac_f32_e32 v85, v108, v44
	v_add_f32_e32 v90, v90, v108
	v_fmac_f32_e32 v94, v108, v35
	v_add_f32_e32 v82, v82, v110
	v_fmac_f32_e32 v86, v110, v43
	v_add_f32_e32 v89, v89, v110
	v_fmac_f32_e32 v93, v110, v36
	v_add_f32_e32 v83, v83, v105
	v_fmac_f32_e32 v87, v105, v46
	v_add_f32_e32 v91, v91, v107
	v_fmac_f32_e32 v95, v107, v38
	v_add_f32_e32 v88, v88, v109
	v_fmac_f32_e32 v92, v109, v41
	v_add_f32_e32 v89, v89, v111
	v_fmac_f32_e32 v93, v111, v44
	v_add_f32_e32 v90, v90, v111
	v_fmac_f32_e32 v94, v111, v43
	v_pk_add_f32 v[88:89], v[88:89], v[104:105] op_sel_hi:[1,0]
	v_pk_fma_f32 v[92:93], v[104:105], v[42:43], v[92:93] op_sel:[0,1,0] op_sel_hi:[0,0,1]
	v_pk_add_f32 v[90:91], v[90:91], v[106:107] op_sel_hi:[1,0]
	v_pk_fma_f32 v[94:95], v[106:107], v[44:45], v[94:95] op_sel:[0,1,0] op_sel_hi:[0,0,1]
	s_nop 0
	v_add_f32_e32 v91, v91, v96
	v_fmac_f32_e32 v95, v96, v46
	v_rcp_f32_e32 v96, v72
	v_rcp_f32_e32 v97, v73
	v_rcp_f32_e32 v98, v74
	v_rcp_f32_e64 v99, v75
	v_pk_mul_f32 v[76:77], v[76:77], s[34:35]
	v_pk_mul_f32 v[78:79], v[78:79], s[34:35]
	v_pk_mul_f32 v[76:77], v[76:77], v[96:97]
	v_pk_mul_f32 v[78:79], v[78:79], v[98:99]
	buffer_store_dwordx4 v[76:79], v114, s[12:15], 0 offen offset:2048 sc1
	s_waitcnt vmcnt(5)
	s_nop 0
	v_mov_b32_dpp v48, v52 row_shr:1 row_mask:0xf bank_mask:0xf
	v_mov_b32_dpp v49, v53 row_shr:1 row_mask:0xf bank_mask:0xf
	v_mov_b32_dpp v54, v50 row_shl:1 row_mask:0xf bank_mask:0xf
	v_mov_b32_dpp v55, v51 row_shl:1 row_mask:0xf bank_mask:0xf
	v_pk_mul_f32 v[50:51], v[50:51], s[32:33]
	v_pk_mul_f32 v[52:53], v[52:53], s[32:33]
	v_cndmask_b32_e64 v49, v49, v48, vcc
	v_cndmask_b32_e64 v54, v54, v55, s[16:17]
	v_pk_mul_f32 v[48:49], v[48:49], s[32:33]
	v_pk_mul_f32 v[54:55], v[54:55], s[32:33]
	v_pk_add_f32 v[96:97], v[48:49], v[34:35] neg_lo:[0,1] neg_hi:[0,1]
	v_pk_add_f32 v[98:99], v[50:51], v[34:35] neg_lo:[0,1] neg_hi:[0,1]
	v_pk_add_f32 v[100:101], v[52:53], v[34:35] neg_lo:[0,1] neg_hi:[0,1]
	v_pk_add_f32 v[102:103], v[50:51], v[36:37] neg_lo:[0,1] neg_hi:[0,1]
	v_pk_fma_f32 v[96:97], v[96:97], v[96:97], s[28:29] neg_lo:[1,0,0] neg_hi:[1,0,0]
	v_pk_fma_f32 v[98:99], v[98:99], v[98:99], s[22:23] neg_lo:[1,0,0] neg_hi:[1,0,0]
	v_pk_fma_f32 v[100:101], v[100:101], v[100:101], s[28:29] neg_lo:[1,0,0] neg_hi:[1,0,0]
	v_pk_fma_f32 v[102:103], v[102:103], v[102:103], s[28:29] neg_lo:[1,0,0] neg_hi:[1,0,0]
	v_exp_f32_e32 v96, v96
	v_exp_f32_e32 v97, v97
	v_exp_f32_e32 v98, v98
	v_exp_f32_e32 v99, v99
	v_exp_f32_e32 v100, v100
	v_exp_f32_e32 v101, v101
	v_exp_f32_e32 v102, v102
	v_exp_f32_e32 v103, v103
	v_pk_add_f32 v[104:105], v[52:53], v[36:37] neg_lo:[0,1] neg_hi:[0,1]
	v_pk_add_f32 v[106:107], v[54:55], v[36:37] neg_lo:[0,1] neg_hi:[0,1]
	v_pk_add_f32 v[108:109], v[50:51], v[34:35] op_sel:[1,0] op_sel_hi:[0,1] neg_lo:[0,1] neg_hi:[0,1]
	v_pk_add_f32 v[110:111], v[52:53], v[36:37] op_sel:[1,0] op_sel_hi:[0,1] neg_lo:[0,1] neg_hi:[0,1]
	v_pk_fma_f32 v[104:105], v[104:105], v[104:105], s[22:23] neg_lo:[1,0,0] neg_hi:[1,0,0]
	v_pk_fma_f32 v[106:107], v[106:107], v[106:107], s[28:29] neg_lo:[1,0,0] neg_hi:[1,0,0]
	v_pk_fma_f32 v[108:109], v[108:109], v[108:109], s[26:27] neg_lo:[1,0,0] neg_hi:[1,0,0]
	v_pk_fma_f32 v[110:111], v[110:111], v[110:111], s[26:27] neg_lo:[1,0,0] neg_hi:[1,0,0]
	v_exp_f32_e32 v104, v104
	v_exp_f32_e32 v105, v105
	v_exp_f32_e32 v106, v106
	v_exp_f32_e32 v107, v107
	v_exp_f32_e32 v108, v108
	v_exp_f32_e32 v109, v109
	v_exp_f32_e32 v110, v110
	v_exp_f32_e32 v111, v111
	v_pk_add_f32 v[80:81], v[80:81], v[96:97]
	v_pk_fma_f32 v[84:85], v[96:97], v[48:49], v[84:85]
	v_pk_add_f32 v[82:83], v[82:83], v[102:103]
	v_pk_add_f32 v[80:81], v[80:81], v[98:99]
	v_pk_fma_f32 v[84:85], v[98:99], v[50:51], v[84:85]
	v_pk_fma_f32 v[86:87], v[102:103], v[50:51], v[86:87]
	v_pk_add_f32 v[80:81], v[80:81], v[100:101]
	v_pk_fma_f32 v[84:85], v[100:101], v[52:53], v[84:85]
	v_pk_add_f32 v[96:97], v[48:49], v[42:43] neg_lo:[0,1] neg_hi:[0,1]
	v_pk_add_f32 v[98:99], v[50:51], v[42:43] neg_lo:[0,1] neg_hi:[0,1]
	v_pk_add_f32 v[100:101], v[52:53], v[42:43] neg_lo:[0,1] neg_hi:[0,1]
	v_pk_add_f32 v[102:103], v[50:51], v[44:45] neg_lo:[0,1] neg_hi:[0,1]
	v_pk_fma_f32 v[96:97], v[96:97], v[96:97], s[26:27] neg_lo:[1,0,0] neg_hi:[1,0,0]
	v_pk_fma_f32 v[98:99], v[98:99], v[98:99], s[20:21] neg_lo:[1,0,0] neg_hi:[1,0,0]
	v_pk_fma_f32 v[100:101], v[100:101], v[100:101], s[26:27] neg_lo:[1,0,0] neg_hi:[1,0,0]
	v_pk_fma_f32 v[102:103], v[102:103], v[102:103], s[26:27] neg_lo:[1,0,0] neg_hi:[1,0,0]
	v_exp_f32_e32 v96, v96
	v_exp_f32_e32 v97, v97
	v_exp_f32_e32 v98, v98
	v_exp_f32_e32 v99, v99
	v_exp_f32_e32 v100, v100
	v_exp_f32_e32 v101, v101
	v_exp_f32_e32 v102, v102
	v_exp_f32_e32 v103, v103
	v_pk_add_f32 v[82:83], v[82:83], v[104:105]
	v_pk_fma_f32 v[86:87], v[104:105], v[52:53], v[86:87]
	v_pk_add_f32 v[80:81], v[80:81], v[108:109]
	v_pk_add_f32 v[82:83], v[82:83], v[106:107]
	v_pk_fma_f32 v[86:87], v[106:107], v[54:55], v[86:87]
	v_pk_fma_f32 v[84:85], v[108:109], v[50:51], v[84:85] op_sel:[0,1,0] op_sel_hi:[1,0,1]
	v_pk_add_f32 v[82:83], v[82:83], v[110:111]
	v_pk_fma_f32 v[86:87], v[110:111], v[52:53], v[86:87] op_sel:[0,1,0] op_sel_hi:[1,0,1]
	v_pk_add_f32 v[104:105], v[52:53], v[44:45] neg_lo:[0,1] neg_hi:[0,1]
	v_pk_add_f32 v[106:107], v[54:55], v[44:45] neg_lo:[0,1] neg_hi:[0,1]
	v_pk_add_f32 v[108:109], v[50:51], v[42:43] op_sel:[1,0] op_sel_hi:[0,1] neg_lo:[0,1] neg_hi:[0,1]
	v_pk_add_f32 v[110:111], v[52:53], v[44:45] op_sel:[1,0] op_sel_hi:[0,1] neg_lo:[0,1] neg_hi:[0,1]
	v_pk_fma_f32 v[104:105], v[104:105], v[104:105], s[20:21] neg_lo:[1,0,0] neg_hi:[1,0,0]
	v_pk_fma_f32 v[106:107], v[106:107], v[106:107], s[26:27] neg_lo:[1,0,0] neg_hi:[1,0,0]
	v_pk_fma_f32 v[108:109], v[108:109], v[108:109], s[24:25] neg_lo:[1,0,0] neg_hi:[1,0,0]
	v_pk_fma_f32 v[110:111], v[110:111], v[110:111], s[24:25] neg_lo:[1,0,0] neg_hi:[1,0,0]
	v_exp_f32_e32 v104, v104
	v_exp_f32_e32 v105, v105
	v_exp_f32_e32 v106, v106
	v_exp_f32_e32 v107, v107
	v_exp_f32_e32 v108, v108
	v_exp_f32_e32 v109, v109
	v_exp_f32_e32 v110, v110
	v_exp_f32_e32 v111, v111
	v_pk_add_f32 v[88:89], v[88:89], v[96:97]
	v_pk_fma_f32 v[92:93], v[96:97], v[48:49], v[92:93]
	v_pk_add_f32 v[90:91], v[90:91], v[102:103]
	v_pk_add_f32 v[88:89], v[88:89], v[98:99]
	v_pk_fma_f32 v[92:93], v[98:99], v[50:51], v[92:93]
	v_pk_fma_f32 v[94:95], v[102:103], v[50:51], v[94:95]
	v_pk_add_f32 v[88:89], v[88:89], v[100:101]
	v_pk_fma_f32 v[92:93], v[100:101], v[52:53], v[92:93]
	v_sub_f32_e32 v96, v49, v34
	v_sub_f32_e32 v98, v52, v35
	v_sub_f32_e32 v100, v51, v36
	v_sub_f32_e32 v102, v54, v37
	v_sub_f32_e32 v97, v49, v42
	v_sub_f32_e32 v99, v52, v43
	v_sub_f32_e32 v101, v51, v44
	v_sub_f32_e32 v103, v54, v45
	v_fma_f32 v96, -v96, v96, s26
	v_fma_f32 v98, -v98, v98, s26
	v_fma_f32 v100, -v100, v100, s26
	v_fma_f32 v102, -v102, v102, s26
	v_fma_f32 v97, -v97, v97, s24
	v_fma_f32 v99, -v99, v99, s24
	v_fma_f32 v101, -v101, v101, s24
	v_fma_f32 v103, -v103, v103, s24
	v_exp_f32_e32 v96, v96
	v_exp_f32_e32 v98, v98
	v_exp_f32_e32 v100, v100
	v_exp_f32_e32 v102, v102
	v_exp_f32_e32 v97, v97
	v_exp_f32_e32 v99, v99
	v_exp_f32_e32 v101, v101
	v_exp_f32_e32 v103, v103
	v_pk_add_f32 v[90:91], v[90:91], v[104:105]
	v_pk_fma_f32 v[94:95], v[104:105], v[52:53], v[94:95]
	v_pk_add_f32 v[88:89], v[88:89], v[108:109]
	v_pk_add_f32 v[90:91], v[90:91], v[106:107]
	v_pk_fma_f32 v[94:95], v[106:107], v[54:55], v[94:95]
	v_pk_fma_f32 v[92:93], v[108:109], v[50:51], v[92:93] op_sel:[0,1,0] op_sel_hi:[1,0,1]
	v_pk_add_f32 v[90:91], v[90:91], v[110:111]
	v_pk_fma_f32 v[94:95], v[110:111], v[52:53], v[94:95] op_sel:[0,1,0] op_sel_hi:[1,0,1]
	v_add_f32_e32 v80, v80, v96
	v_fmac_f32_e32 v84, v96, v49
	v_add_f32_e32 v81, v81, v98
	v_fmac_f32_e32 v85, v98, v52
	v_add_f32_e32 v82, v82, v100
	v_fmac_f32_e32 v86, v100, v51
	v_add_f32_e32 v83, v83, v102
	v_fmac_f32_e32 v87, v102, v54
	v_add_f32_e32 v88, v88, v97
	v_fmac_f32_e32 v92, v97, v49
	v_add_f32_e32 v89, v89, v99
	v_fmac_f32_e32 v93, v99, v52
	v_add_f32_e32 v90, v90, v101
	v_fmac_f32_e32 v94, v101, v51
	v_add_f32_e32 v91, v91, v103
	v_fmac_f32_e32 v95, v103, v54
	v_rcp_f32_e32 v96, v80
	v_rcp_f32_e32 v97, v81
	v_rcp_f32_e32 v98, v82
	v_rcp_f32_e32 v99, v83
	v_pk_mul_f32 v[84:85], v[84:85], s[34:35]
	v_pk_mul_f32 v[86:87], v[86:87], s[34:35]
	v_pk_mul_f32 v[84:85], v[84:85], v[96:97]
	v_pk_mul_f32 v[86:87], v[86:87], v[98:99]
	buffer_store_dwordx4 v[84:87], v119, s[12:15], 0 offen sc1
	s_waitcnt vmcnt(3)
	s_nop 0
	v_mov_b32_dpp v56, v60 row_shr:1 row_mask:0xf bank_mask:0xf
	v_mov_b32_dpp v57, v61 row_shr:1 row_mask:0xf bank_mask:0xf
	v_mov_b32_dpp v62, v58 row_shl:1 row_mask:0xf bank_mask:0xf
	v_mov_b32_dpp v63, v59 row_shl:1 row_mask:0xf bank_mask:0xf
	v_pk_mul_f32 v[58:59], v[58:59], s[32:33]
	v_pk_mul_f32 v[60:61], v[60:61], s[32:33]
	v_cndmask_b32_e64 v57, v57, v56, vcc
	v_cndmask_b32_e64 v62, v62, v63, s[16:17]
	v_pk_mul_f32 v[56:57], v[56:57], s[32:33]
	v_pk_mul_f32 v[62:63], v[62:63], s[32:33]
	v_pk_add_f32 v[96:97], v[56:57], v[42:43] neg_lo:[0,1] neg_hi:[0,1]
	v_pk_add_f32 v[98:99], v[58:59], v[42:43] neg_lo:[0,1] neg_hi:[0,1]
	v_pk_add_f32 v[100:101], v[60:61], v[42:43] neg_lo:[0,1] neg_hi:[0,1]
	v_pk_add_f32 v[102:103], v[58:59], v[44:45] neg_lo:[0,1] neg_hi:[0,1]
	v_pk_fma_f32 v[96:97], v[96:97], v[96:97], s[28:29] neg_lo:[1,0,0] neg_hi:[1,0,0]
	v_pk_fma_f32 v[98:99], v[98:99], v[98:99], s[22:23] neg_lo:[1,0,0] neg_hi:[1,0,0]
	v_pk_fma_f32 v[100:101], v[100:101], v[100:101], s[28:29] neg_lo:[1,0,0] neg_hi:[1,0,0]
	v_pk_fma_f32 v[102:103], v[102:103], v[102:103], s[28:29] neg_lo:[1,0,0] neg_hi:[1,0,0]
	v_exp_f32_e32 v96, v96
	v_exp_f32_e32 v97, v97
	v_exp_f32_e32 v98, v98
	v_exp_f32_e32 v99, v99
	v_exp_f32_e32 v100, v100
	v_exp_f32_e32 v101, v101
	v_exp_f32_e32 v102, v102
	v_exp_f32_e32 v103, v103
	v_pk_add_f32 v[104:105], v[60:61], v[44:45] neg_lo:[0,1] neg_hi:[0,1]
	v_pk_add_f32 v[106:107], v[62:63], v[44:45] neg_lo:[0,1] neg_hi:[0,1]
	v_pk_add_f32 v[108:109], v[58:59], v[42:43] op_sel:[1,0] op_sel_hi:[0,1] neg_lo:[0,1] neg_hi:[0,1]
	v_pk_add_f32 v[110:111], v[60:61], v[44:45] op_sel:[1,0] op_sel_hi:[0,1] neg_lo:[0,1] neg_hi:[0,1]
	v_pk_fma_f32 v[104:105], v[104:105], v[104:105], s[22:23] neg_lo:[1,0,0] neg_hi:[1,0,0]
	v_pk_fma_f32 v[106:107], v[106:107], v[106:107], s[28:29] neg_lo:[1,0,0] neg_hi:[1,0,0]
	v_pk_fma_f32 v[108:109], v[108:109], v[108:109], s[26:27] neg_lo:[1,0,0] neg_hi:[1,0,0]
	v_pk_fma_f32 v[110:111], v[110:111], v[110:111], s[26:27] neg_lo:[1,0,0] neg_hi:[1,0,0]
	v_exp_f32_e32 v104, v104
	v_exp_f32_e32 v105, v105
	v_exp_f32_e32 v106, v106
	v_exp_f32_e32 v107, v107
	v_exp_f32_e32 v108, v108
	v_exp_f32_e32 v109, v109
	v_exp_f32_e32 v110, v110
	v_exp_f32_e32 v111, v111
	v_pk_add_f32 v[88:89], v[88:89], v[96:97]
	v_pk_fma_f32 v[92:93], v[96:97], v[56:57], v[92:93]
	v_pk_add_f32 v[90:91], v[90:91], v[102:103]
	v_pk_add_f32 v[88:89], v[88:89], v[98:99]
	v_pk_fma_f32 v[92:93], v[98:99], v[58:59], v[92:93]
	v_pk_fma_f32 v[94:95], v[102:103], v[58:59], v[94:95]
	v_pk_add_f32 v[88:89], v[88:89], v[100:101]
	v_pk_fma_f32 v[92:93], v[100:101], v[60:61], v[92:93]
	v_sub_f32_e32 v96, v57, v42
	v_sub_f32_e32 v98, v60, v43
	v_sub_f32_e32 v100, v59, v44
	v_sub_f32_e32 v102, v62, v45
	v_fma_f32 v96, -v96, v96, s26
	v_fma_f32 v98, -v98, v98, s26
	v_fma_f32 v100, -v100, v100, s26
	v_fma_f32 v102, -v102, v102, s26
	v_exp_f32_e32 v96, v96
	v_exp_f32_e32 v98, v98
	v_exp_f32_e32 v100, v100
	v_exp_f32_e32 v102, v102
	v_pk_add_f32 v[90:91], v[90:91], v[104:105]
	v_pk_fma_f32 v[94:95], v[104:105], v[60:61], v[94:95]
	v_pk_add_f32 v[88:89], v[88:89], v[108:109]
	v_pk_add_f32 v[90:91], v[90:91], v[106:107]
	v_pk_fma_f32 v[94:95], v[106:107], v[62:63], v[94:95]
	v_pk_fma_f32 v[92:93], v[108:109], v[58:59], v[92:93] op_sel:[0,1,0] op_sel_hi:[1,0,1]
	v_pk_add_f32 v[90:91], v[90:91], v[110:111]
	v_pk_fma_f32 v[94:95], v[110:111], v[60:61], v[94:95] op_sel:[0,1,0] op_sel_hi:[1,0,1]
	v_add_f32_e32 v88, v88, v96
	v_fmac_f32_e32 v92, v96, v57
	v_add_f32_e32 v89, v89, v98
	v_fmac_f32_e32 v93, v98, v60
	v_add_f32_e32 v90, v90, v100
	v_fmac_f32_e32 v94, v100, v59
	v_add_f32_e32 v91, v91, v102
	v_fmac_f32_e32 v95, v102, v62
	v_rcp_f32_e32 v96, v88
	v_rcp_f32_e32 v97, v89
	v_rcp_f32_e32 v98, v90
	v_rcp_f32_e32 v99, v91
	v_pk_mul_f32 v[92:93], v[92:93], s[34:35]
	v_pk_mul_f32 v[94:95], v[94:95], s[34:35]
	v_pk_mul_f32 v[92:93], v[92:93], v[96:97]
	v_pk_mul_f32 v[94:95], v[94:95], v[98:99]
	buffer_store_dwordx4 v[92:95], v119, s[12:15], 0 offen offset:2048 sc1
	s_endpgm
